# P3 expert-weight conversion loops hand-written: three item buffers per wave (two items of loads in flight), short scalar item decode
# baseline (speedup 1.0000x reference)
; __device__ __forceinline__ bool titem_group(int& it, TItem& t, const float* W, size_t wstride, int nmat, int K, int N, const float* gain, float scale, void* WT, size_t tstride_bytes, int mode, int fp8) {
;     const int nblk = N / 64, per = (K / 64) * nblk, tot = per * nmat;
;     if (it >= tot) { it -= tot; return false; }
;     const int mat = it / per, r = it % per, k0 = 64 * (r / nblk), n0 = 64 * (r % nblk), esz = (fp8 == 1) ? 1 : 2;
;     const int drow0 = (mode == 0) ? n0 : (256 * (n0 / 128) + (n0 % 128) + (mode == 2 ? 128 : 0));
;     t.src = W + (size_t)mat * wstride + (size_t)k0 * N + n0; t.gain = gain ? gain + k0 : nullptr;
;     t.dst = (unsigned char*)WT + (size_t)mat * tstride_bytes + ((size_t)drow0 * K + k0) * esz; t.ldw = N; t.ldwt = K * esz; t.fp8 = fp8; t.scale = scale; return true;
; }
; __device__ __forceinline__ void titem_load(const TItem& t, f32x4 (&v)[2][8], f32x4 (&g)[2], int lane) {
;     const int n4 = lane & 7, kr = lane >> 3;
;     const float* gp = t.gain ? t.gain : t.src;
; #pragma unroll
;     for (int h = 0; h < 2; ++h)
; #pragma unroll
;         for (int i = 0; i < 8; ++i) v[h][i] = *(const f32x4*)(t.src + (size_t)(8 * kr + i) * t.ldw + 32 * h + 4 * n4);
;     g[0] = *(const f32x4*)(gp + 8 * kr); g[1] = *(const f32x4*)(gp + 8 * kr + 4);
; }
.LBB0_438:
	s_load_dwordx2 s[0:1], s[94:95], 0xe8
	s_waitcnt lgkmcnt(0)
	s_cmp_lt_i32 s0, 4
	s_cselect_b64 s[2:3], -1, 0
	s_cmp_gt_i32 s1, 3
	s_cselect_b64 s[0:1], -1, 0
	v_writelane_b32 v254, s2, 35
	s_and_b64 s[0:1], s[2:3], s[0:1]
	s_cmpk_lt_i32 s93, 0x100
	v_writelane_b32 v254, s3, 36
	s_cselect_b64 s[2:3], -1, 0
	v_writelane_b32 v254, s2, 37
	s_andn2_b64 vcc, exec, s[0:1]
	s_lshl_b32 s0, s85, 5
	v_writelane_b32 v254, s3, 38
	v_writelane_b32 v254, s0, 39
	s_cbranch_vccnz .LBB0_1083
	v_writelane_b32 v254, s97, 40
	s_bitcmp0_b32 s93, 3
	v_readlane_b32 s0, v254, 12
	s_cselect_b64 s[12:13], -1, 0
	v_readlane_b32 s1, v254, 13
	s_mov_b32 s4, s0
	s_cmp_lt_i32 s0, 0x15000
	s_cselect_b64 s[0:1], -1, 0
	s_cmpk_lt_i32 s4, 0x7000
	s_cselect_b64 s[2:3], -1, 0
	v_writelane_b32 v254, s2, 41
	s_cmpk_gt_i32 s4, 0x6fff
	v_mbcnt_lo_u32_b32 v0, -1, 0
	v_writelane_b32 v254, s3, 42
	s_cselect_b64 s[2:3], -1, 0
	v_writelane_b32 v254, s2, 43
	v_mbcnt_hi_u32_b32 v202, -1, v0
	v_cndmask_b32_e64 v0, 0, 1, s[0:1]
	v_writelane_b32 v254, s3, 44
	s_add_i32 s2, s4, 0xffff9000
	v_writelane_b32 v254, s2, 45
	s_mul_hi_i32 s2, s4, 0x92492493
	s_add_i32 s2, s2, s4
	s_lshr_b32 s3, s2, 31
	s_ashr_i32 s2, s2, 11
	s_add_i32 s3, s2, s3
	s_mul_i32 s2, s3, 0xe00
	s_sub_i32 s2, s4, s2
	s_mul_i32 s4, s2, 0x4925
	s_lshr_b32 s5, s4, 31
	s_ashr_i32 s4, s4, 21
	s_add_i32 s4, s4, s5
	s_mul_i32 s5, s4, 0x70
	s_sub_i32 s2, s2, s5
	s_sext_i32_i16 s5, s2
	s_bfe_u32 s6, s2, 0x10007
	s_lshl_b32 s10, s5, 6
	s_add_i32 s2, s2, s6
	s_bfe_u32 s5, s5, 0x70012
	s_bfe_i32 s2, s2, 0x80000
	s_add_i32 s5, s10, s5
	s_lshl_b32 s8, s4, 6
	s_sext_i32_i16 s2, s2
	s_and_b32 s5, s5, 0xff80
	s_lshl_b32 s2, s2, 7
	s_sub_i32 s5, s10, s5
	s_ashr_i32 s9, s8, 31
	s_and_b32 s2, s2, 0xffffff00
	s_sext_i32_i16 s5, s5
	v_writelane_b32 v254, s8, 46
	s_add_i32 s2, s2, s5
	s_ashr_i32 s11, s10, 31
	v_writelane_b32 v254, s9, 47
	s_mul_hi_i32 s69, s3, 0x3800000
	s_mul_i32 s70, s3, 0x3800000
	v_writelane_b32 v254, s10, 48
	s_mul_hi_i32 s65, s3, 0x1c00000
	s_mul_i32 s68, s3, 0x1c00000
	s_ashr_i32 s3, s2, 31
	v_writelane_b32 v254, s11, 49
	s_lshl_b64 s[2:3], s[2:3], 11
	v_writelane_b32 v254, s2, 50
	v_cmp_ne_u32_e64 s[0:1], 1, v0
	s_mul_i32 s71, s4, 0x1c0000
	v_writelane_b32 v254, s3, 51
	v_writelane_b32 v254, s12, 52
	s_mul_hi_i32 s72, s8, 0x7000
	s_mov_b64 s[66:67], s[94:95]
	v_writelane_b32 v254, s13, 53
	v_writelane_b32 v254, s0, 54
	s_and_b64 vcc, exec, s[12:13]
	s_nop 0
	v_writelane_b32 v254, s1, 55
	s_cbranch_vccnz .LBB0_580
	v_readlane_b32 s0, v254, 54
	v_readlane_b32 s1, v254, 55
	s_and_b64 vcc, exec, s[0:1]
	s_cbranch_vccnz .LBB0_579
	s_load_dwordx2 s[2:3], s[66:67], 0xb0
	s_load_dwordx2 s[4:5], s[66:67], 0xc0
	s_load_dwordx2 s[6:7], s[66:67], 0xc8
	s_load_dwordx2 s[8:9], s[66:67], 0xe0
	v_readlane_b32 s25, v254, 12
	v_mbcnt_lo_u32_b32 v239, -1, 0
	v_mbcnt_hi_u32_b32 v239, -1, v239
	v_and_b32_e32 v237, 7, v239
	v_lshrrev_b32_e32 v203, 3, v239
	v_mul_u32_u24_e32 v220, 0x38000, v203
	v_lshl_add_u32 v220, v237, 4, v220
	v_lshlrev_b32_e32 v221, 16, v203
	v_lshl_add_u32 v221, v237, 4, v221
	v_lshlrev_b32_e32 v222, 5, v203
	v_lshlrev_b32_e32 v223, 13, v237
	v_lshl_add_u32 v223, v203, 3, v223
	v_mul_u32_u24_e32 v224, 0x7000, v237
	v_lshl_add_u32 v224, v203, 3, v224
	v_mov_b32_e32 v225, 0x43e00000
	s_mov_b32 s33, 0xc3e00000
	s_waitcnt lgkmcnt(0)
	s_add_u32 s8, s8, 0xb000000
	s_addc_u32 s9, s9, 0
	s_mov_b32 s35, 0
	s_lshl_b32 s37, s35, 11
	s_add_i32 s37, s37, s25
	s_lshr_b32 s45, s37, 9
	s_mul_i32 s45, s45, 0x2493
	s_lshr_b32 s45, s45, 16
	s_mul_i32 s51, s45, 0xe00
	s_sub_i32 s50, s37, s51
	s_lshr_b32 s51, s50, 4
	s_mul_i32 s51, s51, 0x2493
	s_lshr_b32 s51, s51, 16
	s_mul_i32 s53, s51, 0x70
	s_sub_i32 s52, s50, s53
	s_and_b32 s53, s45, 7
	s_lshr_b32 s60, s45, 3
	s_cmp_lg_u32 s60, 0
	s_cselect_b32 s46, s6, s4
	s_cselect_b32 s47, s7, s5
	s_mul_i32 s63, s53, 0x3800000
	s_add_u32 s46, s46, s63
	s_addc_u32 s47, s47, 0
	s_mul_i32 s63, s51, 0x1c0000
	s_lshl_b32 s37, s52, 8
	s_add_i32 s63, s63, s37
	s_add_u32 s46, s46, s63
	s_addc_u32 s47, s47, 0
	s_lshl_b32 s63, s51, 8
	s_add_u32 s48, s2, s63
	s_addc_u32 s49, s3, 0
	s_mul_i32 s63, s53, 0x1c00000
	s_lshr_b32 s37, s52, 1
	s_lshl_b32 s37, s37, 19
	s_add_i32 s63, s63, s37
	s_and_b32 s37, s52, 1
	s_lshl_b32 s37, s37, 17
	s_add_i32 s63, s63, s37
	s_lshl_b32 s37, s60, 18
	s_add_i32 s63, s63, s37
	s_lshl_b32 s37, s51, 6
	s_add_i32 s63, s63, s37
	s_add_u32 s38, s8, s63
	s_addc_u32 s39, s9, 0
	global_load_dwordx4 v[0:3], v220, s[46:47]
	global_load_dwordx4 v[32:35], v220, s[46:47] offset:128
	v_add_u32_e32 v238, 0x7000, v220
	global_load_dwordx4 v[4:7], v238, s[46:47]
	global_load_dwordx4 v[36:39], v238, s[46:47] offset:128
	v_add_u32_e32 v238, 0xe000, v220
	global_load_dwordx4 v[8:11], v238, s[46:47]
	global_load_dwordx4 v[40:43], v238, s[46:47] offset:128
	v_add_u32_e32 v238, 0x15000, v220
	global_load_dwordx4 v[12:15], v238, s[46:47]
	global_load_dwordx4 v[44:47], v238, s[46:47] offset:128
	v_add_u32_e32 v238, 0x1c000, v220
	global_load_dwordx4 v[16:19], v238, s[46:47]
	global_load_dwordx4 v[48:51], v238, s[46:47] offset:128
	v_add_u32_e32 v238, 0x23000, v220
	global_load_dwordx4 v[20:23], v238, s[46:47]
	global_load_dwordx4 v[52:55], v238, s[46:47] offset:128
	v_add_u32_e32 v238, 0x2a000, v220
	global_load_dwordx4 v[24:27], v238, s[46:47]
	global_load_dwordx4 v[56:59], v238, s[46:47] offset:128
	v_add_u32_e32 v238, 0x31000, v220
	global_load_dwordx4 v[28:31], v238, s[46:47]
	global_load_dwordx4 v[60:63], v238, s[46:47] offset:128
	global_load_dwordx4 v[192:195], v222, s[48:49]
	global_load_dwordx4 v[196:199], v222, s[48:49] offset:16
	s_mov_b32 s35, 1
	s_lshl_b32 s37, s35, 11
; __device__ __forceinline__ bool titem_group(int& it, TItem& t, const float* W, size_t wstride, int nmat, int K, int N, const float* gain, float scale, void* WT, size_t tstride_bytes, int mode, int fp8) {
;     const int nblk = N / 64, per = (K / 64) * nblk, tot = per * nmat;
;     if (it >= tot) { it -= tot; return false; }
;     const int mat = it / per, r = it % per, k0 = 64 * (r / nblk), n0 = 64 * (r % nblk), esz = (fp8 == 1) ? 1 : 2;
;     const int drow0 = (mode == 0) ? n0 : (256 * (n0 / 128) + (n0 % 128) + (mode == 2 ? 128 : 0));
;     t.src = W + (size_t)mat * wstride + (size_t)k0 * N + n0; t.gain = gain ? gain + k0 : nullptr;
;     t.dst = (unsigned char*)WT + (size_t)mat * tstride_bytes + ((size_t)drow0 * K + k0) * esz; t.ldw = N; t.ldwt = K * esz; t.fp8 = fp8; t.scale = scale; return true;
; }
; __device__ __forceinline__ void titem_load(const TItem& t, f32x4 (&v)[2][8], f32x4 (&g)[2], int lane) {
;     const int n4 = lane & 7, kr = lane >> 3;
;     const float* gp = t.gain ? t.gain : t.src;
; #pragma unroll
;     for (int h = 0; h < 2; ++h)
; #pragma unroll
;         for (int i = 0; i < 8; ++i) v[h][i] = *(const f32x4*)(t.src + (size_t)(8 * kr + i) * t.ldw + 32 * h + 4 * n4);
;     g[0] = *(const f32x4*)(gp + 8 * kr); g[1] = *(const f32x4*)(gp + 8 * kr + 4);
; }
	s_add_i32 s37, s37, s25
	s_lshr_b32 s45, s37, 9
	s_mul_i32 s45, s45, 0x2493
	s_lshr_b32 s45, s45, 16
	s_mul_i32 s51, s45, 0xe00
	s_sub_i32 s50, s37, s51
	s_lshr_b32 s51, s50, 4
	s_mul_i32 s51, s51, 0x2493
	s_lshr_b32 s51, s51, 16
	s_mul_i32 s53, s51, 0x70
	s_sub_i32 s52, s50, s53
	s_and_b32 s53, s45, 7
	s_lshr_b32 s60, s45, 3
	s_cmp_lg_u32 s60, 0
	s_cselect_b32 s46, s6, s4
	s_cselect_b32 s47, s7, s5
	s_mul_i32 s63, s53, 0x3800000
	s_add_u32 s46, s46, s63
	s_addc_u32 s47, s47, 0
	s_mul_i32 s63, s51, 0x1c0000
	s_lshl_b32 s37, s52, 8
	s_add_i32 s63, s63, s37
	s_add_u32 s46, s46, s63
	s_addc_u32 s47, s47, 0
	s_lshl_b32 s63, s51, 8
	s_add_u32 s48, s2, s63
	s_addc_u32 s49, s3, 0
	s_mul_i32 s63, s53, 0x1c00000
	s_lshr_b32 s37, s52, 1
	s_lshl_b32 s37, s37, 19
	s_add_i32 s63, s63, s37
	s_and_b32 s37, s52, 1
	s_lshl_b32 s37, s37, 17
	s_add_i32 s63, s63, s37
	s_lshl_b32 s37, s60, 18
	s_add_i32 s63, s63, s37
	s_lshl_b32 s37, s51, 6
	s_add_i32 s63, s63, s37
	s_add_u32 s40, s8, s63
	s_addc_u32 s41, s9, 0
	global_load_dwordx4 v[64:67], v220, s[46:47]
	global_load_dwordx4 v[96:99], v220, s[46:47] offset:128
	v_add_u32_e32 v238, 0x7000, v220
	global_load_dwordx4 v[68:71], v238, s[46:47]
	global_load_dwordx4 v[100:103], v238, s[46:47] offset:128
	v_add_u32_e32 v238, 0xe000, v220
	global_load_dwordx4 v[72:75], v238, s[46:47]
	global_load_dwordx4 v[104:107], v238, s[46:47] offset:128
	v_add_u32_e32 v238, 0x15000, v220
	global_load_dwordx4 v[76:79], v238, s[46:47]
	global_load_dwordx4 v[108:111], v238, s[46:47] offset:128
	v_add_u32_e32 v238, 0x1c000, v220
	global_load_dwordx4 v[80:83], v238, s[46:47]
	global_load_dwordx4 v[112:115], v238, s[46:47] offset:128
	v_add_u32_e32 v238, 0x23000, v220
	global_load_dwordx4 v[84:87], v238, s[46:47]
	global_load_dwordx4 v[116:119], v238, s[46:47] offset:128
	v_add_u32_e32 v238, 0x2a000, v220
	global_load_dwordx4 v[88:91], v238, s[46:47]
	global_load_dwordx4 v[120:123], v238, s[46:47] offset:128
	v_add_u32_e32 v238, 0x31000, v220
	global_load_dwordx4 v[92:95], v238, s[46:47]
	global_load_dwordx4 v[124:127], v238, s[46:47] offset:128
	global_load_dwordx4 v[204:207], v222, s[48:49]
	global_load_dwordx4 v[208:211], v222, s[48:49] offset:16
	s_mov_b32 s35, 2
	s_lshl_b32 s37, s35, 11
	s_add_i32 s37, s37, s25
	s_lshr_b32 s45, s37, 9
	s_mul_i32 s45, s45, 0x2493
	s_lshr_b32 s45, s45, 16
	s_mul_i32 s51, s45, 0xe00
	s_sub_i32 s50, s37, s51
	s_lshr_b32 s51, s50, 4
	s_mul_i32 s51, s51, 0x2493
	s_lshr_b32 s51, s51, 16
	s_mul_i32 s53, s51, 0x70
	s_sub_i32 s52, s50, s53
	s_and_b32 s53, s45, 7
	s_lshr_b32 s60, s45, 3
	s_cmp_lg_u32 s60, 0
	s_cselect_b32 s46, s6, s4
	s_cselect_b32 s47, s7, s5
	s_mul_i32 s63, s53, 0x3800000
	s_add_u32 s46, s46, s63
	s_addc_u32 s47, s47, 0
	s_mul_i32 s63, s51, 0x1c0000
	s_lshl_b32 s37, s52, 8
	s_add_i32 s63, s63, s37
	s_add_u32 s46, s46, s63
	s_addc_u32 s47, s47, 0
	s_lshl_b32 s63, s51, 8
	s_add_u32 s48, s2, s63
	s_addc_u32 s49, s3, 0
	s_mul_i32 s63, s53, 0x1c00000
	s_lshr_b32 s37, s52, 1
	s_lshl_b32 s37, s37, 19
	s_add_i32 s63, s63, s37
	s_and_b32 s37, s52, 1
	s_lshl_b32 s37, s37, 17
	s_add_i32 s63, s63, s37
	s_lshl_b32 s37, s60, 18
	s_add_i32 s63, s63, s37
	s_lshl_b32 s37, s51, 6
	s_add_i32 s63, s63, s37
	s_add_u32 s42, s8, s63
	s_addc_u32 s43, s9, 0
	global_load_dwordx4 v[128:131], v220, s[46:47]
	global_load_dwordx4 v[160:163], v220, s[46:47] offset:128
	v_add_u32_e32 v238, 0x7000, v220
	global_load_dwordx4 v[132:135], v238, s[46:47]
	global_load_dwordx4 v[164:167], v238, s[46:47] offset:128
	v_add_u32_e32 v238, 0xe000, v220
	global_load_dwordx4 v[136:139], v238, s[46:47]
	global_load_dwordx4 v[168:171], v238, s[46:47] offset:128
	v_add_u32_e32 v238, 0x15000, v220
	global_load_dwordx4 v[140:143], v238, s[46:47]
	global_load_dwordx4 v[172:175], v238, s[46:47] offset:128
	v_add_u32_e32 v238, 0x1c000, v220
	global_load_dwordx4 v[144:147], v238, s[46:47]
	global_load_dwordx4 v[176:179], v238, s[46:47] offset:128
	v_add_u32_e32 v238, 0x23000, v220
	global_load_dwordx4 v[148:151], v238, s[46:47]
	global_load_dwordx4 v[180:183], v238, s[46:47] offset:128
	v_add_u32_e32 v238, 0x2a000, v220
	global_load_dwordx4 v[152:155], v238, s[46:47]
	global_load_dwordx4 v[184:187], v238, s[46:47] offset:128
	v_add_u32_e32 v238, 0x31000, v220
	global_load_dwordx4 v[156:159], v238, s[46:47]
	global_load_dwordx4 v[188:191], v238, s[46:47] offset:128
	global_load_dwordx4 v[212:215], v222, s[48:49]
	global_load_dwordx4 v[216:219], v222, s[48:49] offset:16
	s_waitcnt vmcnt(36)
; __device__ __forceinline__ unsigned pk4_fp8(float a, float b, float c, float d) {
;     a = __builtin_amdgcn_fmed3f(a, -448.f, 448.f); b = __builtin_amdgcn_fmed3f(b, -448.f, 448.f); c = __builtin_amdgcn_fmed3f(c, -448.f, 448.f); d = __builtin_amdgcn_fmed3f(d, -448.f, 448.f);
;     unsigned w = 0u; w = __builtin_amdgcn_cvt_pk_fp8_f32(a, b, w, false); w = __builtin_amdgcn_cvt_pk_fp8_f32(c, d, w, true); return w;
; }
; __device__ __forceinline__ void titem_process(const TItem& t, const f32x4 (&v)[2][8], const f32x4 (&g)[2], int lane) {
;     const int n4 = lane & 7, kr = lane >> 3;
;     float s[8];
; #pragma unroll
;     for (int j = 0; j < 8; ++j) s[j] = t.gain ? g[j >> 2][j & 3] * t.scale : t.scale;
;     if (t.fp8 == 1) {
; #pragma unroll
;         for (int h = 0; h < 2; ++h)
; #pragma unroll
;             for (int i = 0; i < 4; ++i) { u32x2 o; o.x = epi::pk4_fp8(v[h][0][i] * s[0], v[h][1][i] * s[1], v[h][2][i] * s[2], v[h][3][i] * s[3]); o.y = epi::pk4_fp8(v[h][4][i] * s[4], v[h][5][i] * s[5], v[h][6][i] * s[6], v[h][7][i] * s[7]);
;                 __builtin_nontemporal_store(o, (u32x2*)(t.dst + (size_t)(32 * h + 4 * n4 + i) * t.ldwt + 8 * kr)); }
	v_mul_f32_e32 v226, 0x43800000, v192
	v_mul_f32_e32 v227, 0x43800000, v193
	v_mul_f32_e32 v228, 0x43800000, v194
	v_mul_f32_e32 v229, 0x43800000, v195
	v_mul_f32_e32 v230, 0x43800000, v196
	v_mul_f32_e32 v231, 0x43800000, v197
	v_mul_f32_e32 v232, 0x43800000, v198
	v_mul_f32_e32 v233, 0x43800000, v199
	v_pk_mul_f32 v[0:1], v[0:1], v[226:227] op_sel:[0,0] op_sel_hi:[1,0]
	v_pk_mul_f32 v[4:5], v[4:5], v[226:227] op_sel:[0,1] op_sel_hi:[1,1]
	v_pk_mul_f32 v[8:9], v[8:9], v[228:229] op_sel:[0,0] op_sel_hi:[1,0]
	v_pk_mul_f32 v[12:13], v[12:13], v[228:229] op_sel:[0,1] op_sel_hi:[1,1]
	v_pk_mul_f32 v[16:17], v[16:17], v[230:231] op_sel:[0,0] op_sel_hi:[1,0]
	v_pk_mul_f32 v[20:21], v[20:21], v[230:231] op_sel:[0,1] op_sel_hi:[1,1]
	v_pk_mul_f32 v[24:25], v[24:25], v[232:233] op_sel:[0,0] op_sel_hi:[1,0]
	v_pk_mul_f32 v[28:29], v[28:29], v[232:233] op_sel:[0,1] op_sel_hi:[1,1]
	v_pk_mul_f32 v[2:3], v[2:3], v[226:227] op_sel:[0,0] op_sel_hi:[1,0]
	v_pk_mul_f32 v[6:7], v[6:7], v[226:227] op_sel:[0,1] op_sel_hi:[1,1]
	v_pk_mul_f32 v[10:11], v[10:11], v[228:229] op_sel:[0,0] op_sel_hi:[1,0]
	v_pk_mul_f32 v[14:15], v[14:15], v[228:229] op_sel:[0,1] op_sel_hi:[1,1]
	v_pk_mul_f32 v[18:19], v[18:19], v[230:231] op_sel:[0,0] op_sel_hi:[1,0]
	v_pk_mul_f32 v[22:23], v[22:23], v[230:231] op_sel:[0,1] op_sel_hi:[1,1]
	v_pk_mul_f32 v[26:27], v[26:27], v[232:233] op_sel:[0,0] op_sel_hi:[1,0]
	v_pk_mul_f32 v[30:31], v[30:31], v[232:233] op_sel:[0,1] op_sel_hi:[1,1]
	v_pk_mul_f32 v[32:33], v[32:33], v[226:227] op_sel:[0,0] op_sel_hi:[1,0]
	v_pk_mul_f32 v[36:37], v[36:37], v[226:227] op_sel:[0,1] op_sel_hi:[1,1]
	v_pk_mul_f32 v[40:41], v[40:41], v[228:229] op_sel:[0,0] op_sel_hi:[1,0]
	v_pk_mul_f32 v[44:45], v[44:45], v[228:229] op_sel:[0,1] op_sel_hi:[1,1]
	v_pk_mul_f32 v[48:49], v[48:49], v[230:231] op_sel:[0,0] op_sel_hi:[1,0]
	v_pk_mul_f32 v[52:53], v[52:53], v[230:231] op_sel:[0,1] op_sel_hi:[1,1]
	v_pk_mul_f32 v[56:57], v[56:57], v[232:233] op_sel:[0,0] op_sel_hi:[1,0]
	v_pk_mul_f32 v[60:61], v[60:61], v[232:233] op_sel:[0,1] op_sel_hi:[1,1]
	v_pk_mul_f32 v[34:35], v[34:35], v[226:227] op_sel:[0,0] op_sel_hi:[1,0]
	v_pk_mul_f32 v[38:39], v[38:39], v[226:227] op_sel:[0,1] op_sel_hi:[1,1]
	v_pk_mul_f32 v[42:43], v[42:43], v[228:229] op_sel:[0,0] op_sel_hi:[1,0]
	v_pk_mul_f32 v[46:47], v[46:47], v[228:229] op_sel:[0,1] op_sel_hi:[1,1]
	v_pk_mul_f32 v[50:51], v[50:51], v[230:231] op_sel:[0,0] op_sel_hi:[1,0]
	v_pk_mul_f32 v[54:55], v[54:55], v[230:231] op_sel:[0,1] op_sel_hi:[1,1]
	v_pk_mul_f32 v[58:59], v[58:59], v[232:233] op_sel:[0,0] op_sel_hi:[1,0]
	v_pk_mul_f32 v[62:63], v[62:63], v[232:233] op_sel:[0,1] op_sel_hi:[1,1]
	v_med3_f32 v0, v0, s33, v225
	v_med3_f32 v1, v1, s33, v225
	v_med3_f32 v2, v2, s33, v225
	v_med3_f32 v3, v3, s33, v225
	v_med3_f32 v4, v4, s33, v225
	v_med3_f32 v5, v5, s33, v225
	v_med3_f32 v6, v6, s33, v225
	v_med3_f32 v7, v7, s33, v225
	v_med3_f32 v8, v8, s33, v225
	v_med3_f32 v9, v9, s33, v225
	v_med3_f32 v10, v10, s33, v225
	v_med3_f32 v11, v11, s33, v225
	v_med3_f32 v12, v12, s33, v225
	v_med3_f32 v13, v13, s33, v225
	v_med3_f32 v14, v14, s33, v225
	v_med3_f32 v15, v15, s33, v225
	v_med3_f32 v16, v16, s33, v225
	v_med3_f32 v17, v17, s33, v225
	v_med3_f32 v18, v18, s33, v225
	v_med3_f32 v19, v19, s33, v225
	v_med3_f32 v20, v20, s33, v225
	v_med3_f32 v21, v21, s33, v225
	v_med3_f32 v22, v22, s33, v225
	v_med3_f32 v23, v23, s33, v225
	v_med3_f32 v24, v24, s33, v225
	v_med3_f32 v25, v25, s33, v225
	v_med3_f32 v26, v26, s33, v225
	v_med3_f32 v27, v27, s33, v225
	v_med3_f32 v28, v28, s33, v225
	v_med3_f32 v29, v29, s33, v225
	v_med3_f32 v30, v30, s33, v225
	v_med3_f32 v31, v31, s33, v225
	v_med3_f32 v32, v32, s33, v225
	v_med3_f32 v33, v33, s33, v225
	v_med3_f32 v34, v34, s33, v225
	v_med3_f32 v35, v35, s33, v225
	v_med3_f32 v36, v36, s33, v225
	v_med3_f32 v37, v37, s33, v225
	v_med3_f32 v38, v38, s33, v225
	v_med3_f32 v39, v39, s33, v225
	v_med3_f32 v40, v40, s33, v225
	v_med3_f32 v41, v41, s33, v225
	v_med3_f32 v42, v42, s33, v225
	v_med3_f32 v43, v43, s33, v225
	v_med3_f32 v44, v44, s33, v225
	v_med3_f32 v45, v45, s33, v225
	v_med3_f32 v46, v46, s33, v225
	v_med3_f32 v47, v47, s33, v225
	v_med3_f32 v48, v48, s33, v225
	v_med3_f32 v49, v49, s33, v225
	v_med3_f32 v50, v50, s33, v225
	v_med3_f32 v51, v51, s33, v225
	v_med3_f32 v52, v52, s33, v225
	v_med3_f32 v53, v53, s33, v225
	v_med3_f32 v54, v54, s33, v225
	v_med3_f32 v55, v55, s33, v225
	v_med3_f32 v56, v56, s33, v225
	v_med3_f32 v57, v57, s33, v225
	v_med3_f32 v58, v58, s33, v225
	v_med3_f32 v59, v59, s33, v225
	v_med3_f32 v60, v60, s33, v225
	v_med3_f32 v61, v61, s33, v225
	v_med3_f32 v62, v62, s33, v225
	v_med3_f32 v63, v63, s33, v225
	v_cvt_pk_fp8_f32 v234, v0, v4
	v_cvt_pk_fp8_f32 v235, v16, v20
	v_cvt_pk_fp8_f32 v234, v8, v12 op_sel:[0,0,1]
	v_cvt_pk_fp8_f32 v235, v24, v28 op_sel:[0,0,1]
	s_nop 0
	global_store_dwordx2 v223, v[234:235], s[38:39] nt
	v_cvt_pk_fp8_f32 v236, v1, v5
	v_cvt_pk_fp8_f32 v237, v17, v21
	v_cvt_pk_fp8_f32 v236, v9, v13 op_sel:[0,0,1]
	v_cvt_pk_fp8_f32 v237, v25, v29 op_sel:[0,0,1]
	v_add_u32_e32 v238, 0x800, v223
	global_store_dwordx2 v238, v[236:237], s[38:39] nt
	v_cvt_pk_fp8_f32 v234, v2, v6
	v_cvt_pk_fp8_f32 v235, v18, v22
	v_cvt_pk_fp8_f32 v234, v10, v14 op_sel:[0,0,1]
	v_cvt_pk_fp8_f32 v235, v26, v30 op_sel:[0,0,1]
	v_add_u32_e32 v238, 0x1000, v223
	global_store_dwordx2 v238, v[234:235], s[38:39] nt
	v_cvt_pk_fp8_f32 v236, v3, v7
	v_cvt_pk_fp8_f32 v237, v19, v23
	v_cvt_pk_fp8_f32 v236, v11, v15 op_sel:[0,0,1]
	v_cvt_pk_fp8_f32 v237, v27, v31 op_sel:[0,0,1]
	v_add_u32_e32 v238, 0x1800, v223
	global_store_dwordx2 v238, v[236:237], s[38:39] nt
	v_cvt_pk_fp8_f32 v234, v32, v36
	v_cvt_pk_fp8_f32 v235, v48, v52
	v_cvt_pk_fp8_f32 v234, v40, v44 op_sel:[0,0,1]
	v_cvt_pk_fp8_f32 v235, v56, v60 op_sel:[0,0,1]
	v_add_u32_e32 v238, 0x10000, v223
	global_store_dwordx2 v238, v[234:235], s[38:39] nt
	v_cvt_pk_fp8_f32 v236, v33, v37
	v_cvt_pk_fp8_f32 v237, v49, v53
	v_cvt_pk_fp8_f32 v236, v41, v45 op_sel:[0,0,1]
	v_cvt_pk_fp8_f32 v237, v57, v61 op_sel:[0,0,1]
	v_add_u32_e32 v238, 0x10800, v223
	global_store_dwordx2 v238, v[236:237], s[38:39] nt
	v_cvt_pk_fp8_f32 v234, v34, v38
	v_cvt_pk_fp8_f32 v235, v50, v54
	v_cvt_pk_fp8_f32 v234, v42, v46 op_sel:[0,0,1]
	v_cvt_pk_fp8_f32 v235, v58, v62 op_sel:[0,0,1]
	v_add_u32_e32 v238, 0x11000, v223
	global_store_dwordx2 v238, v[234:235], s[38:39] nt
	v_cvt_pk_fp8_f32 v236, v35, v39
	v_cvt_pk_fp8_f32 v237, v51, v55
	v_cvt_pk_fp8_f32 v236, v43, v47 op_sel:[0,0,1]
	v_cvt_pk_fp8_f32 v237, v59, v63 op_sel:[0,0,1]
	v_add_u32_e32 v238, 0x11800, v223
	global_store_dwordx2 v238, v[236:237], s[38:39] nt
	s_mov_b32 s27, 1
	s_mov_b32 s30, 9
; __device__ __forceinline__ bool titem_group(int& it, TItem& t, const float* W, size_t wstride, int nmat, int K, int N, const float* gain, float scale, void* WT, size_t tstride_bytes, int mode, int fp8) {
;     const int nblk = N / 64, per = (K / 64) * nblk, tot = per * nmat;
;     if (it >= tot) { it -= tot; return false; }
;     const int mat = it / per, r = it % per, k0 = 64 * (r / nblk), n0 = 64 * (r % nblk), esz = (fp8 == 1) ? 1 : 2;
;     const int drow0 = (mode == 0) ? n0 : (256 * (n0 / 128) + (n0 % 128) + (mode == 2 ? 128 : 0));
;     t.src = W + (size_t)mat * wstride + (size_t)k0 * N + n0; t.gain = gain ? gain + k0 : nullptr;
;     t.dst = (unsigned char*)WT + (size_t)mat * tstride_bytes + ((size_t)drow0 * K + k0) * esz; t.ldw = N; t.ldwt = K * esz; t.fp8 = fp8; t.scale = scale; return true;
; }
; __device__ __forceinline__ void titem_load(const TItem& t, f32x4 (&v)[2][8], f32x4 (&g)[2], int lane) {
;     const int n4 = lane & 7, kr = lane >> 3;
;     const float* gp = t.gain ? t.gain : t.src;
; #pragma unroll
;     for (int h = 0; h < 2; ++h)
; #pragma unroll
;         for (int i = 0; i < 8; ++i) v[h][i] = *(const f32x4*)(t.src + (size_t)(8 * kr + i) * t.ldw + 32 * h + 4 * n4);
;     g[0] = *(const f32x4*)(gp + 8 * kr); g[1] = *(const f32x4*)(gp + 8 * kr + 4);
; }
.Lcv1_gu:
	s_add_i32 s35, s27, 2
	s_min_u32 s35, s35, 27
	s_lshl_b32 s37, s35, 11
	s_add_i32 s37, s37, s25
	s_lshr_b32 s45, s37, 9
	s_mul_i32 s45, s45, 0x2493
	s_lshr_b32 s45, s45, 16
	s_mul_i32 s51, s45, 0xe00
	s_sub_i32 s50, s37, s51
	s_lshr_b32 s51, s50, 4
	s_mul_i32 s51, s51, 0x2493
	s_lshr_b32 s51, s51, 16
	s_mul_i32 s53, s51, 0x70
	s_sub_i32 s52, s50, s53
	s_and_b32 s53, s45, 7
	s_lshr_b32 s60, s45, 3
	s_cmp_lg_u32 s60, 0
	s_cselect_b32 s46, s6, s4
	s_cselect_b32 s47, s7, s5
	s_mul_i32 s63, s53, 0x3800000
	s_add_u32 s46, s46, s63
	s_addc_u32 s47, s47, 0
	s_mul_i32 s63, s51, 0x1c0000
	s_lshl_b32 s37, s52, 8
	s_add_i32 s63, s63, s37
	s_add_u32 s46, s46, s63
	s_addc_u32 s47, s47, 0
	s_lshl_b32 s63, s51, 8
	s_add_u32 s48, s2, s63
	s_addc_u32 s49, s3, 0
	s_mul_i32 s63, s53, 0x1c00000
	s_lshr_b32 s37, s52, 1
	s_lshl_b32 s37, s37, 19
	s_add_i32 s63, s63, s37
	s_and_b32 s37, s52, 1
	s_lshl_b32 s37, s37, 17
	s_add_i32 s63, s63, s37
	s_lshl_b32 s37, s60, 18
	s_add_i32 s63, s63, s37
	s_lshl_b32 s37, s51, 6
	s_add_i32 s63, s63, s37
	s_add_u32 s38, s8, s63
	s_addc_u32 s39, s9, 0
	global_load_dwordx4 v[0:3], v220, s[46:47]
	global_load_dwordx4 v[32:35], v220, s[46:47] offset:128
	v_add_u32_e32 v238, 0x7000, v220
	global_load_dwordx4 v[4:7], v238, s[46:47]
	global_load_dwordx4 v[36:39], v238, s[46:47] offset:128
	v_add_u32_e32 v238, 0xe000, v220
	global_load_dwordx4 v[8:11], v238, s[46:47]
	global_load_dwordx4 v[40:43], v238, s[46:47] offset:128
	v_add_u32_e32 v238, 0x15000, v220
	global_load_dwordx4 v[12:15], v238, s[46:47]
	global_load_dwordx4 v[44:47], v238, s[46:47] offset:128
	v_add_u32_e32 v238, 0x1c000, v220
	global_load_dwordx4 v[16:19], v238, s[46:47]
	global_load_dwordx4 v[48:51], v238, s[46:47] offset:128
	v_add_u32_e32 v238, 0x23000, v220
	global_load_dwordx4 v[20:23], v238, s[46:47]
	global_load_dwordx4 v[52:55], v238, s[46:47] offset:128
	v_add_u32_e32 v238, 0x2a000, v220
	global_load_dwordx4 v[24:27], v238, s[46:47]
	global_load_dwordx4 v[56:59], v238, s[46:47] offset:128
	v_add_u32_e32 v238, 0x31000, v220
	global_load_dwordx4 v[28:31], v238, s[46:47]
	global_load_dwordx4 v[60:63], v238, s[46:47] offset:128
	global_load_dwordx4 v[192:195], v222, s[48:49]
	global_load_dwordx4 v[196:199], v222, s[48:49] offset:16
	s_waitcnt vmcnt(44)
	v_mul_f32_e32 v226, 0x43800000, v204
	v_mul_f32_e32 v227, 0x43800000, v205
	v_mul_f32_e32 v228, 0x43800000, v206
	v_mul_f32_e32 v229, 0x43800000, v207
	v_mul_f32_e32 v230, 0x43800000, v208
	v_mul_f32_e32 v231, 0x43800000, v209
	v_mul_f32_e32 v232, 0x43800000, v210
	v_mul_f32_e32 v233, 0x43800000, v211
	v_pk_mul_f32 v[64:65], v[64:65], v[226:227] op_sel:[0,0] op_sel_hi:[1,0]
	v_pk_mul_f32 v[68:69], v[68:69], v[226:227] op_sel:[0,1] op_sel_hi:[1,1]
	v_pk_mul_f32 v[72:73], v[72:73], v[228:229] op_sel:[0,0] op_sel_hi:[1,0]
	v_pk_mul_f32 v[76:77], v[76:77], v[228:229] op_sel:[0,1] op_sel_hi:[1,1]
	v_pk_mul_f32 v[80:81], v[80:81], v[230:231] op_sel:[0,0] op_sel_hi:[1,0]
	v_pk_mul_f32 v[84:85], v[84:85], v[230:231] op_sel:[0,1] op_sel_hi:[1,1]
	v_pk_mul_f32 v[88:89], v[88:89], v[232:233] op_sel:[0,0] op_sel_hi:[1,0]
	v_pk_mul_f32 v[92:93], v[92:93], v[232:233] op_sel:[0,1] op_sel_hi:[1,1]
	v_pk_mul_f32 v[66:67], v[66:67], v[226:227] op_sel:[0,0] op_sel_hi:[1,0]
	v_pk_mul_f32 v[70:71], v[70:71], v[226:227] op_sel:[0,1] op_sel_hi:[1,1]
	v_pk_mul_f32 v[74:75], v[74:75], v[228:229] op_sel:[0,0] op_sel_hi:[1,0]
	v_pk_mul_f32 v[78:79], v[78:79], v[228:229] op_sel:[0,1] op_sel_hi:[1,1]
	v_pk_mul_f32 v[82:83], v[82:83], v[230:231] op_sel:[0,0] op_sel_hi:[1,0]
	v_pk_mul_f32 v[86:87], v[86:87], v[230:231] op_sel:[0,1] op_sel_hi:[1,1]
	v_pk_mul_f32 v[90:91], v[90:91], v[232:233] op_sel:[0,0] op_sel_hi:[1,0]
	v_pk_mul_f32 v[94:95], v[94:95], v[232:233] op_sel:[0,1] op_sel_hi:[1,1]
	v_pk_mul_f32 v[96:97], v[96:97], v[226:227] op_sel:[0,0] op_sel_hi:[1,0]
	v_pk_mul_f32 v[100:101], v[100:101], v[226:227] op_sel:[0,1] op_sel_hi:[1,1]
	v_pk_mul_f32 v[104:105], v[104:105], v[228:229] op_sel:[0,0] op_sel_hi:[1,0]
	v_pk_mul_f32 v[108:109], v[108:109], v[228:229] op_sel:[0,1] op_sel_hi:[1,1]
	v_pk_mul_f32 v[112:113], v[112:113], v[230:231] op_sel:[0,0] op_sel_hi:[1,0]
	v_pk_mul_f32 v[116:117], v[116:117], v[230:231] op_sel:[0,1] op_sel_hi:[1,1]
	v_pk_mul_f32 v[120:121], v[120:121], v[232:233] op_sel:[0,0] op_sel_hi:[1,0]
	v_pk_mul_f32 v[124:125], v[124:125], v[232:233] op_sel:[0,1] op_sel_hi:[1,1]
	v_pk_mul_f32 v[98:99], v[98:99], v[226:227] op_sel:[0,0] op_sel_hi:[1,0]
	v_pk_mul_f32 v[102:103], v[102:103], v[226:227] op_sel:[0,1] op_sel_hi:[1,1]
	v_pk_mul_f32 v[106:107], v[106:107], v[228:229] op_sel:[0,0] op_sel_hi:[1,0]
	v_pk_mul_f32 v[110:111], v[110:111], v[228:229] op_sel:[0,1] op_sel_hi:[1,1]
	v_pk_mul_f32 v[114:115], v[114:115], v[230:231] op_sel:[0,0] op_sel_hi:[1,0]
	v_pk_mul_f32 v[118:119], v[118:119], v[230:231] op_sel:[0,1] op_sel_hi:[1,1]
	v_pk_mul_f32 v[122:123], v[122:123], v[232:233] op_sel:[0,0] op_sel_hi:[1,0]
	v_pk_mul_f32 v[126:127], v[126:127], v[232:233] op_sel:[0,1] op_sel_hi:[1,1]
	v_med3_f32 v64, v64, s33, v225
	v_med3_f32 v65, v65, s33, v225
	v_med3_f32 v66, v66, s33, v225
	v_med3_f32 v67, v67, s33, v225
	v_med3_f32 v68, v68, s33, v225
	v_med3_f32 v69, v69, s33, v225
	v_med3_f32 v70, v70, s33, v225
	v_med3_f32 v71, v71, s33, v225
	v_med3_f32 v72, v72, s33, v225
	v_med3_f32 v73, v73, s33, v225
	v_med3_f32 v74, v74, s33, v225
	v_med3_f32 v75, v75, s33, v225
	v_med3_f32 v76, v76, s33, v225
	v_med3_f32 v77, v77, s33, v225
	v_med3_f32 v78, v78, s33, v225
	v_med3_f32 v79, v79, s33, v225
	v_med3_f32 v80, v80, s33, v225
	v_med3_f32 v81, v81, s33, v225
	v_med3_f32 v82, v82, s33, v225
	v_med3_f32 v83, v83, s33, v225
; __device__ __forceinline__ bool titem_group(int& it, TItem& t, const float* W, size_t wstride, int nmat, int K, int N, const float* gain, float scale, void* WT, size_t tstride_bytes, int mode, int fp8) {
;     const int nblk = N / 64, per = (K / 64) * nblk, tot = per * nmat;
;     if (it >= tot) { it -= tot; return false; }
;     const int mat = it / per, r = it % per, k0 = 64 * (r / nblk), n0 = 64 * (r % nblk), esz = (fp8 == 1) ? 1 : 2;
;     const int drow0 = (mode == 0) ? n0 : (256 * (n0 / 128) + (n0 % 128) + (mode == 2 ? 128 : 0));
;     t.src = W + (size_t)mat * wstride + (size_t)k0 * N + n0; t.gain = gain ? gain + k0 : nullptr;
;     t.dst = (unsigned char*)WT + (size_t)mat * tstride_bytes + ((size_t)drow0 * K + k0) * esz; t.ldw = N; t.ldwt = K * esz; t.fp8 = fp8; t.scale = scale; return true;
; }
; __device__ __forceinline__ void titem_load(const TItem& t, f32x4 (&v)[2][8], f32x4 (&g)[2], int lane) {
;     const int n4 = lane & 7, kr = lane >> 3;
;     const float* gp = t.gain ? t.gain : t.src;
; #pragma unroll
;     for (int h = 0; h < 2; ++h)
; #pragma unroll
;         for (int i = 0; i < 8; ++i) v[h][i] = *(const f32x4*)(t.src + (size_t)(8 * kr + i) * t.ldw + 32 * h + 4 * n4);
;     g[0] = *(const f32x4*)(gp + 8 * kr); g[1] = *(const f32x4*)(gp + 8 * kr + 4);
; }
; __device__ __forceinline__ void titem_process(const TItem& t, const f32x4 (&v)[2][8], const f32x4 (&g)[2], int lane) {
;     const int n4 = lane & 7, kr = lane >> 3;
;     float s[8];
; #pragma unroll
;     for (int j = 0; j < 8; ++j) s[j] = t.gain ? g[j >> 2][j & 3] * t.scale : t.scale;
;     if (t.fp8 == 1) {
; #pragma unroll
;         for (int h = 0; h < 2; ++h)
; #pragma unroll
;             for (int i = 0; i < 4; ++i) { u32x2 o; o.x = epi::pk4_fp8(v[h][0][i] * s[0], v[h][1][i] * s[1], v[h][2][i] * s[2], v[h][3][i] * s[3]); o.y = epi::pk4_fp8(v[h][4][i] * s[4], v[h][5][i] * s[5], v[h][6][i] * s[6], v[h][7][i] * s[7]);
;                 __builtin_nontemporal_store(o, (u32x2*)(t.dst + (size_t)(32 * h + 4 * n4 + i) * t.ldwt + 8 * kr)); }
	v_med3_f32 v84, v84, s33, v225
	v_med3_f32 v85, v85, s33, v225
	v_med3_f32 v86, v86, s33, v225
	v_med3_f32 v87, v87, s33, v225
	v_med3_f32 v88, v88, s33, v225
	v_med3_f32 v89, v89, s33, v225
	v_med3_f32 v90, v90, s33, v225
	v_med3_f32 v91, v91, s33, v225
	v_med3_f32 v92, v92, s33, v225
	v_med3_f32 v93, v93, s33, v225
	v_med3_f32 v94, v94, s33, v225
	v_med3_f32 v95, v95, s33, v225
	v_med3_f32 v96, v96, s33, v225
	v_med3_f32 v97, v97, s33, v225
	v_med3_f32 v98, v98, s33, v225
	v_med3_f32 v99, v99, s33, v225
	v_med3_f32 v100, v100, s33, v225
	v_med3_f32 v101, v101, s33, v225
	v_med3_f32 v102, v102, s33, v225
	v_med3_f32 v103, v103, s33, v225
	v_med3_f32 v104, v104, s33, v225
	v_med3_f32 v105, v105, s33, v225
	v_med3_f32 v106, v106, s33, v225
	v_med3_f32 v107, v107, s33, v225
	v_med3_f32 v108, v108, s33, v225
	v_med3_f32 v109, v109, s33, v225
	v_med3_f32 v110, v110, s33, v225
	v_med3_f32 v111, v111, s33, v225
	v_med3_f32 v112, v112, s33, v225
	v_med3_f32 v113, v113, s33, v225
	v_med3_f32 v114, v114, s33, v225
	v_med3_f32 v115, v115, s33, v225
	v_med3_f32 v116, v116, s33, v225
	v_med3_f32 v117, v117, s33, v225
	v_med3_f32 v118, v118, s33, v225
	v_med3_f32 v119, v119, s33, v225
	v_med3_f32 v120, v120, s33, v225
	v_med3_f32 v121, v121, s33, v225
	v_med3_f32 v122, v122, s33, v225
	v_med3_f32 v123, v123, s33, v225
	v_med3_f32 v124, v124, s33, v225
	v_med3_f32 v125, v125, s33, v225
	v_med3_f32 v126, v126, s33, v225
	v_med3_f32 v127, v127, s33, v225
	v_cvt_pk_fp8_f32 v234, v64, v68
	v_cvt_pk_fp8_f32 v235, v80, v84
	v_cvt_pk_fp8_f32 v234, v72, v76 op_sel:[0,0,1]
	v_cvt_pk_fp8_f32 v235, v88, v92 op_sel:[0,0,1]
	s_nop 0
	global_store_dwordx2 v223, v[234:235], s[40:41] nt
	v_cvt_pk_fp8_f32 v236, v65, v69
	v_cvt_pk_fp8_f32 v237, v81, v85
	v_cvt_pk_fp8_f32 v236, v73, v77 op_sel:[0,0,1]
	v_cvt_pk_fp8_f32 v237, v89, v93 op_sel:[0,0,1]
	v_add_u32_e32 v238, 0x800, v223
	global_store_dwordx2 v238, v[236:237], s[40:41] nt
	v_cvt_pk_fp8_f32 v234, v66, v70
	v_cvt_pk_fp8_f32 v235, v82, v86
	v_cvt_pk_fp8_f32 v234, v74, v78 op_sel:[0,0,1]
	v_cvt_pk_fp8_f32 v235, v90, v94 op_sel:[0,0,1]
	v_add_u32_e32 v238, 0x1000, v223
	global_store_dwordx2 v238, v[234:235], s[40:41] nt
	v_cvt_pk_fp8_f32 v236, v67, v71
	v_cvt_pk_fp8_f32 v237, v83, v87
	v_cvt_pk_fp8_f32 v236, v75, v79 op_sel:[0,0,1]
	v_cvt_pk_fp8_f32 v237, v91, v95 op_sel:[0,0,1]
	v_add_u32_e32 v238, 0x1800, v223
	global_store_dwordx2 v238, v[236:237], s[40:41] nt
	v_cvt_pk_fp8_f32 v234, v96, v100
	v_cvt_pk_fp8_f32 v235, v112, v116
	v_cvt_pk_fp8_f32 v234, v104, v108 op_sel:[0,0,1]
	v_cvt_pk_fp8_f32 v235, v120, v124 op_sel:[0,0,1]
	v_add_u32_e32 v238, 0x10000, v223
	global_store_dwordx2 v238, v[234:235], s[40:41] nt
	v_cvt_pk_fp8_f32 v236, v97, v101
	v_cvt_pk_fp8_f32 v237, v113, v117
	v_cvt_pk_fp8_f32 v236, v105, v109 op_sel:[0,0,1]
	v_cvt_pk_fp8_f32 v237, v121, v125 op_sel:[0,0,1]
	v_add_u32_e32 v238, 0x10800, v223
	global_store_dwordx2 v238, v[236:237], s[40:41] nt
	v_cvt_pk_fp8_f32 v234, v98, v102
	v_cvt_pk_fp8_f32 v235, v114, v118
	v_cvt_pk_fp8_f32 v234, v106, v110 op_sel:[0,0,1]
	v_cvt_pk_fp8_f32 v235, v122, v126 op_sel:[0,0,1]
	v_add_u32_e32 v238, 0x11000, v223
	global_store_dwordx2 v238, v[234:235], s[40:41] nt
	v_cvt_pk_fp8_f32 v236, v99, v103
	v_cvt_pk_fp8_f32 v237, v115, v119
	v_cvt_pk_fp8_f32 v236, v107, v111 op_sel:[0,0,1]
	v_cvt_pk_fp8_f32 v237, v123, v127 op_sel:[0,0,1]
	v_add_u32_e32 v238, 0x11800, v223
	global_store_dwordx2 v238, v[236:237], s[40:41] nt
	s_add_i32 s35, s27, 3
	s_min_u32 s35, s35, 27
	s_lshl_b32 s37, s35, 11
	s_add_i32 s37, s37, s25
	s_lshr_b32 s45, s37, 9
	s_mul_i32 s45, s45, 0x2493
	s_lshr_b32 s45, s45, 16
	s_mul_i32 s51, s45, 0xe00
	s_sub_i32 s50, s37, s51
	s_lshr_b32 s51, s50, 4
	s_mul_i32 s51, s51, 0x2493
	s_lshr_b32 s51, s51, 16
	s_mul_i32 s53, s51, 0x70
	s_sub_i32 s52, s50, s53
	s_and_b32 s53, s45, 7
	s_lshr_b32 s60, s45, 3
	s_cmp_lg_u32 s60, 0
	s_cselect_b32 s46, s6, s4
	s_cselect_b32 s47, s7, s5
	s_mul_i32 s63, s53, 0x3800000
	s_add_u32 s46, s46, s63
	s_addc_u32 s47, s47, 0
	s_mul_i32 s63, s51, 0x1c0000
	s_lshl_b32 s37, s52, 8
	s_add_i32 s63, s63, s37
	s_add_u32 s46, s46, s63
	s_addc_u32 s47, s47, 0
	s_lshl_b32 s63, s51, 8
	s_add_u32 s48, s2, s63
	s_addc_u32 s49, s3, 0
	s_mul_i32 s63, s53, 0x1c00000
	s_lshr_b32 s37, s52, 1
	s_lshl_b32 s37, s37, 19
	s_add_i32 s63, s63, s37
	s_and_b32 s37, s52, 1
	s_lshl_b32 s37, s37, 17
	s_add_i32 s63, s63, s37
	s_lshl_b32 s37, s60, 18
	s_add_i32 s63, s63, s37
	s_lshl_b32 s37, s51, 6
	s_add_i32 s63, s63, s37
	s_add_u32 s40, s8, s63
	s_addc_u32 s41, s9, 0
	global_load_dwordx4 v[64:67], v220, s[46:47]
	global_load_dwordx4 v[96:99], v220, s[46:47] offset:128
	v_add_u32_e32 v238, 0x7000, v220
	global_load_dwordx4 v[68:71], v238, s[46:47]
	global_load_dwordx4 v[100:103], v238, s[46:47] offset:128
	v_add_u32_e32 v238, 0xe000, v220
	global_load_dwordx4 v[72:75], v238, s[46:47]
	global_load_dwordx4 v[104:107], v238, s[46:47] offset:128
	v_add_u32_e32 v238, 0x15000, v220
	global_load_dwordx4 v[76:79], v238, s[46:47]
	global_load_dwordx4 v[108:111], v238, s[46:47] offset:128
	v_add_u32_e32 v238, 0x1c000, v220
	global_load_dwordx4 v[80:83], v238, s[46:47]
	global_load_dwordx4 v[112:115], v238, s[46:47] offset:128
	v_add_u32_e32 v238, 0x23000, v220
	global_load_dwordx4 v[84:87], v238, s[46:47]
	global_load_dwordx4 v[116:119], v238, s[46:47] offset:128
	v_add_u32_e32 v238, 0x2a000, v220
	global_load_dwordx4 v[88:91], v238, s[46:47]
	global_load_dwordx4 v[120:123], v238, s[46:47] offset:128
	v_add_u32_e32 v238, 0x31000, v220
	global_load_dwordx4 v[92:95], v238, s[46:47]
	global_load_dwordx4 v[124:127], v238, s[46:47] offset:128
	global_load_dwordx4 v[204:207], v222, s[48:49]
	global_load_dwordx4 v[208:211], v222, s[48:49] offset:16
	s_waitcnt vmcnt(44)
; __device__ __forceinline__ unsigned pk4_fp8(float a, float b, float c, float d) {
;     a = __builtin_amdgcn_fmed3f(a, -448.f, 448.f); b = __builtin_amdgcn_fmed3f(b, -448.f, 448.f); c = __builtin_amdgcn_fmed3f(c, -448.f, 448.f); d = __builtin_amdgcn_fmed3f(d, -448.f, 448.f);
;     unsigned w = 0u; w = __builtin_amdgcn_cvt_pk_fp8_f32(a, b, w, false); w = __builtin_amdgcn_cvt_pk_fp8_f32(c, d, w, true); return w;
; }
; __device__ __forceinline__ void titem_process(const TItem& t, const f32x4 (&v)[2][8], const f32x4 (&g)[2], int lane) {
;     const int n4 = lane & 7, kr = lane >> 3;
;     float s[8];
; #pragma unroll
;     for (int j = 0; j < 8; ++j) s[j] = t.gain ? g[j >> 2][j & 3] * t.scale : t.scale;
;     if (t.fp8 == 1) {
; #pragma unroll
;         for (int h = 0; h < 2; ++h)
; #pragma unroll
;             for (int i = 0; i < 4; ++i) { u32x2 o; o.x = epi::pk4_fp8(v[h][0][i] * s[0], v[h][1][i] * s[1], v[h][2][i] * s[2], v[h][3][i] * s[3]); o.y = epi::pk4_fp8(v[h][4][i] * s[4], v[h][5][i] * s[5], v[h][6][i] * s[6], v[h][7][i] * s[7]);
;                 __builtin_nontemporal_store(o, (u32x2*)(t.dst + (size_t)(32 * h + 4 * n4 + i) * t.ldwt + 8 * kr)); }
	v_mul_f32_e32 v226, 0x43800000, v212
	v_mul_f32_e32 v227, 0x43800000, v213
	v_mul_f32_e32 v228, 0x43800000, v214
	v_mul_f32_e32 v229, 0x43800000, v215
	v_mul_f32_e32 v230, 0x43800000, v216
	v_mul_f32_e32 v231, 0x43800000, v217
	v_mul_f32_e32 v232, 0x43800000, v218
	v_mul_f32_e32 v233, 0x43800000, v219
	v_pk_mul_f32 v[128:129], v[128:129], v[226:227] op_sel:[0,0] op_sel_hi:[1,0]
	v_pk_mul_f32 v[132:133], v[132:133], v[226:227] op_sel:[0,1] op_sel_hi:[1,1]
	v_pk_mul_f32 v[136:137], v[136:137], v[228:229] op_sel:[0,0] op_sel_hi:[1,0]
	v_pk_mul_f32 v[140:141], v[140:141], v[228:229] op_sel:[0,1] op_sel_hi:[1,1]
	v_pk_mul_f32 v[144:145], v[144:145], v[230:231] op_sel:[0,0] op_sel_hi:[1,0]
	v_pk_mul_f32 v[148:149], v[148:149], v[230:231] op_sel:[0,1] op_sel_hi:[1,1]
	v_pk_mul_f32 v[152:153], v[152:153], v[232:233] op_sel:[0,0] op_sel_hi:[1,0]
	v_pk_mul_f32 v[156:157], v[156:157], v[232:233] op_sel:[0,1] op_sel_hi:[1,1]
	v_pk_mul_f32 v[130:131], v[130:131], v[226:227] op_sel:[0,0] op_sel_hi:[1,0]
	v_pk_mul_f32 v[134:135], v[134:135], v[226:227] op_sel:[0,1] op_sel_hi:[1,1]
	v_pk_mul_f32 v[138:139], v[138:139], v[228:229] op_sel:[0,0] op_sel_hi:[1,0]
	v_pk_mul_f32 v[142:143], v[142:143], v[228:229] op_sel:[0,1] op_sel_hi:[1,1]
	v_pk_mul_f32 v[146:147], v[146:147], v[230:231] op_sel:[0,0] op_sel_hi:[1,0]
	v_pk_mul_f32 v[150:151], v[150:151], v[230:231] op_sel:[0,1] op_sel_hi:[1,1]
	v_pk_mul_f32 v[154:155], v[154:155], v[232:233] op_sel:[0,0] op_sel_hi:[1,0]
	v_pk_mul_f32 v[158:159], v[158:159], v[232:233] op_sel:[0,1] op_sel_hi:[1,1]
	v_pk_mul_f32 v[160:161], v[160:161], v[226:227] op_sel:[0,0] op_sel_hi:[1,0]
	v_pk_mul_f32 v[164:165], v[164:165], v[226:227] op_sel:[0,1] op_sel_hi:[1,1]
	v_pk_mul_f32 v[168:169], v[168:169], v[228:229] op_sel:[0,0] op_sel_hi:[1,0]
	v_pk_mul_f32 v[172:173], v[172:173], v[228:229] op_sel:[0,1] op_sel_hi:[1,1]
	v_pk_mul_f32 v[176:177], v[176:177], v[230:231] op_sel:[0,0] op_sel_hi:[1,0]
	v_pk_mul_f32 v[180:181], v[180:181], v[230:231] op_sel:[0,1] op_sel_hi:[1,1]
	v_pk_mul_f32 v[184:185], v[184:185], v[232:233] op_sel:[0,0] op_sel_hi:[1,0]
	v_pk_mul_f32 v[188:189], v[188:189], v[232:233] op_sel:[0,1] op_sel_hi:[1,1]
	v_pk_mul_f32 v[162:163], v[162:163], v[226:227] op_sel:[0,0] op_sel_hi:[1,0]
	v_pk_mul_f32 v[166:167], v[166:167], v[226:227] op_sel:[0,1] op_sel_hi:[1,1]
	v_pk_mul_f32 v[170:171], v[170:171], v[228:229] op_sel:[0,0] op_sel_hi:[1,0]
	v_pk_mul_f32 v[174:175], v[174:175], v[228:229] op_sel:[0,1] op_sel_hi:[1,1]
	v_pk_mul_f32 v[178:179], v[178:179], v[230:231] op_sel:[0,0] op_sel_hi:[1,0]
	v_pk_mul_f32 v[182:183], v[182:183], v[230:231] op_sel:[0,1] op_sel_hi:[1,1]
	v_pk_mul_f32 v[186:187], v[186:187], v[232:233] op_sel:[0,0] op_sel_hi:[1,0]
	v_pk_mul_f32 v[190:191], v[190:191], v[232:233] op_sel:[0,1] op_sel_hi:[1,1]
	v_med3_f32 v128, v128, s33, v225
	v_med3_f32 v129, v129, s33, v225
	v_med3_f32 v130, v130, s33, v225
	v_med3_f32 v131, v131, s33, v225
	v_med3_f32 v132, v132, s33, v225
	v_med3_f32 v133, v133, s33, v225
	v_med3_f32 v134, v134, s33, v225
	v_med3_f32 v135, v135, s33, v225
	v_med3_f32 v136, v136, s33, v225
	v_med3_f32 v137, v137, s33, v225
	v_med3_f32 v138, v138, s33, v225
	v_med3_f32 v139, v139, s33, v225
	v_med3_f32 v140, v140, s33, v225
	v_med3_f32 v141, v141, s33, v225
	v_med3_f32 v142, v142, s33, v225
	v_med3_f32 v143, v143, s33, v225
	v_med3_f32 v144, v144, s33, v225
	v_med3_f32 v145, v145, s33, v225
	v_med3_f32 v146, v146, s33, v225
	v_med3_f32 v147, v147, s33, v225
	v_med3_f32 v148, v148, s33, v225
	v_med3_f32 v149, v149, s33, v225
	v_med3_f32 v150, v150, s33, v225
	v_med3_f32 v151, v151, s33, v225
	v_med3_f32 v152, v152, s33, v225
	v_med3_f32 v153, v153, s33, v225
	v_med3_f32 v154, v154, s33, v225
	v_med3_f32 v155, v155, s33, v225
	v_med3_f32 v156, v156, s33, v225
	v_med3_f32 v157, v157, s33, v225
	v_med3_f32 v158, v158, s33, v225
	v_med3_f32 v159, v159, s33, v225
	v_med3_f32 v160, v160, s33, v225
	v_med3_f32 v161, v161, s33, v225
	v_med3_f32 v162, v162, s33, v225
	v_med3_f32 v163, v163, s33, v225
	v_med3_f32 v164, v164, s33, v225
	v_med3_f32 v165, v165, s33, v225
	v_med3_f32 v166, v166, s33, v225
	v_med3_f32 v167, v167, s33, v225
	v_med3_f32 v168, v168, s33, v225
	v_med3_f32 v169, v169, s33, v225
	v_med3_f32 v170, v170, s33, v225
	v_med3_f32 v171, v171, s33, v225
	v_med3_f32 v172, v172, s33, v225
	v_med3_f32 v173, v173, s33, v225
	v_med3_f32 v174, v174, s33, v225
	v_med3_f32 v175, v175, s33, v225
	v_med3_f32 v176, v176, s33, v225
	v_med3_f32 v177, v177, s33, v225
	v_med3_f32 v178, v178, s33, v225
	v_med3_f32 v179, v179, s33, v225
	v_med3_f32 v180, v180, s33, v225
	v_med3_f32 v181, v181, s33, v225
	v_med3_f32 v182, v182, s33, v225
	v_med3_f32 v183, v183, s33, v225
	v_med3_f32 v184, v184, s33, v225
	v_med3_f32 v185, v185, s33, v225
	v_med3_f32 v186, v186, s33, v225
	v_med3_f32 v187, v187, s33, v225
	v_med3_f32 v188, v188, s33, v225
	v_med3_f32 v189, v189, s33, v225
	v_med3_f32 v190, v190, s33, v225
	v_med3_f32 v191, v191, s33, v225
	v_cvt_pk_fp8_f32 v234, v128, v132
	v_cvt_pk_fp8_f32 v235, v144, v148
	v_cvt_pk_fp8_f32 v234, v136, v140 op_sel:[0,0,1]
	v_cvt_pk_fp8_f32 v235, v152, v156 op_sel:[0,0,1]
	s_nop 0
	global_store_dwordx2 v223, v[234:235], s[42:43] nt
	v_cvt_pk_fp8_f32 v236, v129, v133
	v_cvt_pk_fp8_f32 v237, v145, v149
	v_cvt_pk_fp8_f32 v236, v137, v141 op_sel:[0,0,1]
	v_cvt_pk_fp8_f32 v237, v153, v157 op_sel:[0,0,1]
	v_add_u32_e32 v238, 0x800, v223
	global_store_dwordx2 v238, v[236:237], s[42:43] nt
	v_cvt_pk_fp8_f32 v234, v130, v134
	v_cvt_pk_fp8_f32 v235, v146, v150
	v_cvt_pk_fp8_f32 v234, v138, v142 op_sel:[0,0,1]
	v_cvt_pk_fp8_f32 v235, v154, v158 op_sel:[0,0,1]
; __device__ __forceinline__ bool titem_group(int& it, TItem& t, const float* W, size_t wstride, int nmat, int K, int N, const float* gain, float scale, void* WT, size_t tstride_bytes, int mode, int fp8) {
;     const int nblk = N / 64, per = (K / 64) * nblk, tot = per * nmat;
;     if (it >= tot) { it -= tot; return false; }
;     const int mat = it / per, r = it % per, k0 = 64 * (r / nblk), n0 = 64 * (r % nblk), esz = (fp8 == 1) ? 1 : 2;
;     const int drow0 = (mode == 0) ? n0 : (256 * (n0 / 128) + (n0 % 128) + (mode == 2 ? 128 : 0));
;     t.src = W + (size_t)mat * wstride + (size_t)k0 * N + n0; t.gain = gain ? gain + k0 : nullptr;
;     t.dst = (unsigned char*)WT + (size_t)mat * tstride_bytes + ((size_t)drow0 * K + k0) * esz; t.ldw = N; t.ldwt = K * esz; t.fp8 = fp8; t.scale = scale; return true;
; }
; __device__ __forceinline__ void titem_load(const TItem& t, f32x4 (&v)[2][8], f32x4 (&g)[2], int lane) {
;     const int n4 = lane & 7, kr = lane >> 3;
;     const float* gp = t.gain ? t.gain : t.src;
; #pragma unroll
;     for (int h = 0; h < 2; ++h)
; #pragma unroll
;         for (int i = 0; i < 8; ++i) v[h][i] = *(const f32x4*)(t.src + (size_t)(8 * kr + i) * t.ldw + 32 * h + 4 * n4);
;     g[0] = *(const f32x4*)(gp + 8 * kr); g[1] = *(const f32x4*)(gp + 8 * kr + 4);
; }
; __device__ __forceinline__ void titem_process(const TItem& t, const f32x4 (&v)[2][8], const f32x4 (&g)[2], int lane) {
;     const int n4 = lane & 7, kr = lane >> 3;
;     float s[8];
; #pragma unroll
;     for (int j = 0; j < 8; ++j) s[j] = t.gain ? g[j >> 2][j & 3] * t.scale : t.scale;
;     if (t.fp8 == 1) {
; #pragma unroll
;         for (int h = 0; h < 2; ++h)
; #pragma unroll
;             for (int i = 0; i < 4; ++i) { u32x2 o; o.x = epi::pk4_fp8(v[h][0][i] * s[0], v[h][1][i] * s[1], v[h][2][i] * s[2], v[h][3][i] * s[3]); o.y = epi::pk4_fp8(v[h][4][i] * s[4], v[h][5][i] * s[5], v[h][6][i] * s[6], v[h][7][i] * s[7]);
;                 __builtin_nontemporal_store(o, (u32x2*)(t.dst + (size_t)(32 * h + 4 * n4 + i) * t.ldwt + 8 * kr)); }
	v_add_u32_e32 v238, 0x1000, v223
	global_store_dwordx2 v238, v[234:235], s[42:43] nt
	v_cvt_pk_fp8_f32 v236, v131, v135
	v_cvt_pk_fp8_f32 v237, v147, v151
	v_cvt_pk_fp8_f32 v236, v139, v143 op_sel:[0,0,1]
	v_cvt_pk_fp8_f32 v237, v155, v159 op_sel:[0,0,1]
	v_add_u32_e32 v238, 0x1800, v223
	global_store_dwordx2 v238, v[236:237], s[42:43] nt
	v_cvt_pk_fp8_f32 v234, v160, v164
	v_cvt_pk_fp8_f32 v235, v176, v180
	v_cvt_pk_fp8_f32 v234, v168, v172 op_sel:[0,0,1]
	v_cvt_pk_fp8_f32 v235, v184, v188 op_sel:[0,0,1]
	v_add_u32_e32 v238, 0x10000, v223
	global_store_dwordx2 v238, v[234:235], s[42:43] nt
	v_cvt_pk_fp8_f32 v236, v161, v165
	v_cvt_pk_fp8_f32 v237, v177, v181
	v_cvt_pk_fp8_f32 v236, v169, v173 op_sel:[0,0,1]
	v_cvt_pk_fp8_f32 v237, v185, v189 op_sel:[0,0,1]
	v_add_u32_e32 v238, 0x10800, v223
	global_store_dwordx2 v238, v[236:237], s[42:43] nt
	v_cvt_pk_fp8_f32 v234, v162, v166
	v_cvt_pk_fp8_f32 v235, v178, v182
	v_cvt_pk_fp8_f32 v234, v170, v174 op_sel:[0,0,1]
	v_cvt_pk_fp8_f32 v235, v186, v190 op_sel:[0,0,1]
	v_add_u32_e32 v238, 0x11000, v223
	global_store_dwordx2 v238, v[234:235], s[42:43] nt
	v_cvt_pk_fp8_f32 v236, v163, v167
	v_cvt_pk_fp8_f32 v237, v179, v183
	v_cvt_pk_fp8_f32 v236, v171, v175 op_sel:[0,0,1]
	v_cvt_pk_fp8_f32 v237, v187, v191 op_sel:[0,0,1]
	v_add_u32_e32 v238, 0x11800, v223
	global_store_dwordx2 v238, v[236:237], s[42:43] nt
	s_add_i32 s35, s27, 4
	s_min_u32 s35, s35, 27
	s_lshl_b32 s37, s35, 11
	s_add_i32 s37, s37, s25
	s_lshr_b32 s45, s37, 9
	s_mul_i32 s45, s45, 0x2493
	s_lshr_b32 s45, s45, 16
	s_mul_i32 s51, s45, 0xe00
	s_sub_i32 s50, s37, s51
	s_lshr_b32 s51, s50, 4
	s_mul_i32 s51, s51, 0x2493
	s_lshr_b32 s51, s51, 16
	s_mul_i32 s53, s51, 0x70
	s_sub_i32 s52, s50, s53
	s_and_b32 s53, s45, 7
	s_lshr_b32 s60, s45, 3
	s_cmp_lg_u32 s60, 0
	s_cselect_b32 s46, s6, s4
	s_cselect_b32 s47, s7, s5
	s_mul_i32 s63, s53, 0x3800000
	s_add_u32 s46, s46, s63
	s_addc_u32 s47, s47, 0
	s_mul_i32 s63, s51, 0x1c0000
	s_lshl_b32 s37, s52, 8
	s_add_i32 s63, s63, s37
	s_add_u32 s46, s46, s63
	s_addc_u32 s47, s47, 0
	s_lshl_b32 s63, s51, 8
	s_add_u32 s48, s2, s63
	s_addc_u32 s49, s3, 0
	s_mul_i32 s63, s53, 0x1c00000
	s_lshr_b32 s37, s52, 1
	s_lshl_b32 s37, s37, 19
	s_add_i32 s63, s63, s37
	s_and_b32 s37, s52, 1
	s_lshl_b32 s37, s37, 17
	s_add_i32 s63, s63, s37
	s_lshl_b32 s37, s60, 18
	s_add_i32 s63, s63, s37
	s_lshl_b32 s37, s51, 6
	s_add_i32 s63, s63, s37
	s_add_u32 s42, s8, s63
	s_addc_u32 s43, s9, 0
	global_load_dwordx4 v[128:131], v220, s[46:47]
	global_load_dwordx4 v[160:163], v220, s[46:47] offset:128
	v_add_u32_e32 v238, 0x7000, v220
	global_load_dwordx4 v[132:135], v238, s[46:47]
	global_load_dwordx4 v[164:167], v238, s[46:47] offset:128
	v_add_u32_e32 v238, 0xe000, v220
	global_load_dwordx4 v[136:139], v238, s[46:47]
	global_load_dwordx4 v[168:171], v238, s[46:47] offset:128
	v_add_u32_e32 v238, 0x15000, v220
	global_load_dwordx4 v[140:143], v238, s[46:47]
	global_load_dwordx4 v[172:175], v238, s[46:47] offset:128
	v_add_u32_e32 v238, 0x1c000, v220
	global_load_dwordx4 v[144:147], v238, s[46:47]
	global_load_dwordx4 v[176:179], v238, s[46:47] offset:128
	v_add_u32_e32 v238, 0x23000, v220
	global_load_dwordx4 v[148:151], v238, s[46:47]
	global_load_dwordx4 v[180:183], v238, s[46:47] offset:128
	v_add_u32_e32 v238, 0x2a000, v220
	global_load_dwordx4 v[152:155], v238, s[46:47]
	global_load_dwordx4 v[184:187], v238, s[46:47] offset:128
	v_add_u32_e32 v238, 0x31000, v220
	global_load_dwordx4 v[156:159], v238, s[46:47]
	global_load_dwordx4 v[188:191], v238, s[46:47] offset:128
	global_load_dwordx4 v[212:215], v222, s[48:49]
	global_load_dwordx4 v[216:219], v222, s[48:49] offset:16
	s_waitcnt vmcnt(44)
	v_mul_f32_e32 v226, 0x43800000, v192
	v_mul_f32_e32 v227, 0x43800000, v193
	v_mul_f32_e32 v228, 0x43800000, v194
	v_mul_f32_e32 v229, 0x43800000, v195
	v_mul_f32_e32 v230, 0x43800000, v196
	v_mul_f32_e32 v231, 0x43800000, v197
	v_mul_f32_e32 v232, 0x43800000, v198
	v_mul_f32_e32 v233, 0x43800000, v199
	v_pk_mul_f32 v[0:1], v[0:1], v[226:227] op_sel:[0,0] op_sel_hi:[1,0]
	v_pk_mul_f32 v[4:5], v[4:5], v[226:227] op_sel:[0,1] op_sel_hi:[1,1]
	v_pk_mul_f32 v[8:9], v[8:9], v[228:229] op_sel:[0,0] op_sel_hi:[1,0]
	v_pk_mul_f32 v[12:13], v[12:13], v[228:229] op_sel:[0,1] op_sel_hi:[1,1]
	v_pk_mul_f32 v[16:17], v[16:17], v[230:231] op_sel:[0,0] op_sel_hi:[1,0]
	v_pk_mul_f32 v[20:21], v[20:21], v[230:231] op_sel:[0,1] op_sel_hi:[1,1]
	v_pk_mul_f32 v[24:25], v[24:25], v[232:233] op_sel:[0,0] op_sel_hi:[1,0]
	v_pk_mul_f32 v[28:29], v[28:29], v[232:233] op_sel:[0,1] op_sel_hi:[1,1]
	v_pk_mul_f32 v[2:3], v[2:3], v[226:227] op_sel:[0,0] op_sel_hi:[1,0]
	v_pk_mul_f32 v[6:7], v[6:7], v[226:227] op_sel:[0,1] op_sel_hi:[1,1]
	v_pk_mul_f32 v[10:11], v[10:11], v[228:229] op_sel:[0,0] op_sel_hi:[1,0]
	v_pk_mul_f32 v[14:15], v[14:15], v[228:229] op_sel:[0,1] op_sel_hi:[1,1]
	v_pk_mul_f32 v[18:19], v[18:19], v[230:231] op_sel:[0,0] op_sel_hi:[1,0]
	v_pk_mul_f32 v[22:23], v[22:23], v[230:231] op_sel:[0,1] op_sel_hi:[1,1]
	v_pk_mul_f32 v[26:27], v[26:27], v[232:233] op_sel:[0,0] op_sel_hi:[1,0]
	v_pk_mul_f32 v[30:31], v[30:31], v[232:233] op_sel:[0,1] op_sel_hi:[1,1]
	v_pk_mul_f32 v[32:33], v[32:33], v[226:227] op_sel:[0,0] op_sel_hi:[1,0]
	v_pk_mul_f32 v[36:37], v[36:37], v[226:227] op_sel:[0,1] op_sel_hi:[1,1]
	v_pk_mul_f32 v[40:41], v[40:41], v[228:229] op_sel:[0,0] op_sel_hi:[1,0]
	v_pk_mul_f32 v[44:45], v[44:45], v[228:229] op_sel:[0,1] op_sel_hi:[1,1]
	v_pk_mul_f32 v[48:49], v[48:49], v[230:231] op_sel:[0,0] op_sel_hi:[1,0]
	v_pk_mul_f32 v[52:53], v[52:53], v[230:231] op_sel:[0,1] op_sel_hi:[1,1]
	v_pk_mul_f32 v[56:57], v[56:57], v[232:233] op_sel:[0,0] op_sel_hi:[1,0]
; __device__ __forceinline__ void titem_process(const TItem& t, const f32x4 (&v)[2][8], const f32x4 (&g)[2], int lane) {
;     const int n4 = lane & 7, kr = lane >> 3;
;     float s[8];
; #pragma unroll
;     for (int j = 0; j < 8; ++j) s[j] = t.gain ? g[j >> 2][j & 3] * t.scale : t.scale;
;     if (t.fp8 == 1) {
; #pragma unroll
;         for (int h = 0; h < 2; ++h)
; #pragma unroll
;             for (int i = 0; i < 4; ++i) { u32x2 o; o.x = epi::pk4_fp8(v[h][0][i] * s[0], v[h][1][i] * s[1], v[h][2][i] * s[2], v[h][3][i] * s[3]); o.y = epi::pk4_fp8(v[h][4][i] * s[4], v[h][5][i] * s[5], v[h][6][i] * s[6], v[h][7][i] * s[7]);
;                 __builtin_nontemporal_store(o, (u32x2*)(t.dst + (size_t)(32 * h + 4 * n4 + i) * t.ldwt + 8 * kr)); }
	v_pk_mul_f32 v[60:61], v[60:61], v[232:233] op_sel:[0,1] op_sel_hi:[1,1]
	v_pk_mul_f32 v[34:35], v[34:35], v[226:227] op_sel:[0,0] op_sel_hi:[1,0]
	v_pk_mul_f32 v[38:39], v[38:39], v[226:227] op_sel:[0,1] op_sel_hi:[1,1]
	v_pk_mul_f32 v[42:43], v[42:43], v[228:229] op_sel:[0,0] op_sel_hi:[1,0]
	v_pk_mul_f32 v[46:47], v[46:47], v[228:229] op_sel:[0,1] op_sel_hi:[1,1]
	v_pk_mul_f32 v[50:51], v[50:51], v[230:231] op_sel:[0,0] op_sel_hi:[1,0]
	v_pk_mul_f32 v[54:55], v[54:55], v[230:231] op_sel:[0,1] op_sel_hi:[1,1]
	v_pk_mul_f32 v[58:59], v[58:59], v[232:233] op_sel:[0,0] op_sel_hi:[1,0]
	v_pk_mul_f32 v[62:63], v[62:63], v[232:233] op_sel:[0,1] op_sel_hi:[1,1]
	v_med3_f32 v0, v0, s33, v225
	v_med3_f32 v1, v1, s33, v225
	v_med3_f32 v2, v2, s33, v225
	v_med3_f32 v3, v3, s33, v225
	v_med3_f32 v4, v4, s33, v225
	v_med3_f32 v5, v5, s33, v225
	v_med3_f32 v6, v6, s33, v225
	v_med3_f32 v7, v7, s33, v225
	v_med3_f32 v8, v8, s33, v225
	v_med3_f32 v9, v9, s33, v225
	v_med3_f32 v10, v10, s33, v225
	v_med3_f32 v11, v11, s33, v225
	v_med3_f32 v12, v12, s33, v225
	v_med3_f32 v13, v13, s33, v225
	v_med3_f32 v14, v14, s33, v225
	v_med3_f32 v15, v15, s33, v225
	v_med3_f32 v16, v16, s33, v225
	v_med3_f32 v17, v17, s33, v225
	v_med3_f32 v18, v18, s33, v225
	v_med3_f32 v19, v19, s33, v225
	v_med3_f32 v20, v20, s33, v225
	v_med3_f32 v21, v21, s33, v225
	v_med3_f32 v22, v22, s33, v225
	v_med3_f32 v23, v23, s33, v225
	v_med3_f32 v24, v24, s33, v225
	v_med3_f32 v25, v25, s33, v225
	v_med3_f32 v26, v26, s33, v225
	v_med3_f32 v27, v27, s33, v225
	v_med3_f32 v28, v28, s33, v225
	v_med3_f32 v29, v29, s33, v225
	v_med3_f32 v30, v30, s33, v225
	v_med3_f32 v31, v31, s33, v225
	v_med3_f32 v32, v32, s33, v225
	v_med3_f32 v33, v33, s33, v225
	v_med3_f32 v34, v34, s33, v225
	v_med3_f32 v35, v35, s33, v225
	v_med3_f32 v36, v36, s33, v225
	v_med3_f32 v37, v37, s33, v225
	v_med3_f32 v38, v38, s33, v225
	v_med3_f32 v39, v39, s33, v225
	v_med3_f32 v40, v40, s33, v225
	v_med3_f32 v41, v41, s33, v225
	v_med3_f32 v42, v42, s33, v225
	v_med3_f32 v43, v43, s33, v225
	v_med3_f32 v44, v44, s33, v225
	v_med3_f32 v45, v45, s33, v225
	v_med3_f32 v46, v46, s33, v225
	v_med3_f32 v47, v47, s33, v225
	v_med3_f32 v48, v48, s33, v225
	v_med3_f32 v49, v49, s33, v225
	v_med3_f32 v50, v50, s33, v225
	v_med3_f32 v51, v51, s33, v225
	v_med3_f32 v52, v52, s33, v225
	v_med3_f32 v53, v53, s33, v225
	v_med3_f32 v54, v54, s33, v225
	v_med3_f32 v55, v55, s33, v225
	v_med3_f32 v56, v56, s33, v225
	v_med3_f32 v57, v57, s33, v225
	v_med3_f32 v58, v58, s33, v225
	v_med3_f32 v59, v59, s33, v225
	v_med3_f32 v60, v60, s33, v225
	v_med3_f32 v61, v61, s33, v225
	v_med3_f32 v62, v62, s33, v225
	v_med3_f32 v63, v63, s33, v225
	v_cvt_pk_fp8_f32 v234, v0, v4
	v_cvt_pk_fp8_f32 v235, v16, v20
	v_cvt_pk_fp8_f32 v234, v8, v12 op_sel:[0,0,1]
	v_cvt_pk_fp8_f32 v235, v24, v28 op_sel:[0,0,1]
	s_nop 0
	global_store_dwordx2 v223, v[234:235], s[38:39] nt
	v_cvt_pk_fp8_f32 v236, v1, v5
	v_cvt_pk_fp8_f32 v237, v17, v21
	v_cvt_pk_fp8_f32 v236, v9, v13 op_sel:[0,0,1]
	v_cvt_pk_fp8_f32 v237, v25, v29 op_sel:[0,0,1]
	v_add_u32_e32 v238, 0x800, v223
	global_store_dwordx2 v238, v[236:237], s[38:39] nt
	v_cvt_pk_fp8_f32 v234, v2, v6
	v_cvt_pk_fp8_f32 v235, v18, v22
	v_cvt_pk_fp8_f32 v234, v10, v14 op_sel:[0,0,1]
	v_cvt_pk_fp8_f32 v235, v26, v30 op_sel:[0,0,1]
	v_add_u32_e32 v238, 0x1000, v223
	global_store_dwordx2 v238, v[234:235], s[38:39] nt
	v_cvt_pk_fp8_f32 v236, v3, v7
	v_cvt_pk_fp8_f32 v237, v19, v23
	v_cvt_pk_fp8_f32 v236, v11, v15 op_sel:[0,0,1]
	v_cvt_pk_fp8_f32 v237, v27, v31 op_sel:[0,0,1]
	v_add_u32_e32 v238, 0x1800, v223
	global_store_dwordx2 v238, v[236:237], s[38:39] nt
	v_cvt_pk_fp8_f32 v234, v32, v36
	v_cvt_pk_fp8_f32 v235, v48, v52
	v_cvt_pk_fp8_f32 v234, v40, v44 op_sel:[0,0,1]
	v_cvt_pk_fp8_f32 v235, v56, v60 op_sel:[0,0,1]
	v_add_u32_e32 v238, 0x10000, v223
	global_store_dwordx2 v238, v[234:235], s[38:39] nt
	v_cvt_pk_fp8_f32 v236, v33, v37
	v_cvt_pk_fp8_f32 v237, v49, v53
	v_cvt_pk_fp8_f32 v236, v41, v45 op_sel:[0,0,1]
	v_cvt_pk_fp8_f32 v237, v57, v61 op_sel:[0,0,1]
	v_add_u32_e32 v238, 0x10800, v223
	global_store_dwordx2 v238, v[236:237], s[38:39] nt
	v_cvt_pk_fp8_f32 v234, v34, v38
	v_cvt_pk_fp8_f32 v235, v50, v54
	v_cvt_pk_fp8_f32 v234, v42, v46 op_sel:[0,0,1]
	v_cvt_pk_fp8_f32 v235, v58, v62 op_sel:[0,0,1]
	v_add_u32_e32 v238, 0x11000, v223
	global_store_dwordx2 v238, v[234:235], s[38:39] nt
	v_cvt_pk_fp8_f32 v236, v35, v39
	v_cvt_pk_fp8_f32 v237, v51, v55
	v_cvt_pk_fp8_f32 v236, v43, v47 op_sel:[0,0,1]
	v_cvt_pk_fp8_f32 v237, v59, v63 op_sel:[0,0,1]
	v_add_u32_e32 v238, 0x11800, v223
	global_store_dwordx2 v238, v[236:237], s[38:39] nt
	s_add_i32 s27, s27, 3
	s_sub_i32 s30, s30, 1
	s_cmp_lg_u32 s30, 0
	s_cbranch_scc1 .Lcv1_gu
; __device__ __forceinline__ bool titem_group(int& it, TItem& t, const float* W, size_t wstride, int nmat, int K, int N, const float* gain, float scale, void* WT, size_t tstride_bytes, int mode, int fp8) {
;     const int nblk = N / 64, per = (K / 64) * nblk, tot = per * nmat;
;     if (it >= tot) { it -= tot; return false; }
;     const int mat = it / per, r = it % per, k0 = 64 * (r / nblk), n0 = 64 * (r % nblk), esz = (fp8 == 1) ? 1 : 2;
;     const int drow0 = (mode == 0) ? n0 : (256 * (n0 / 128) + (n0 % 128) + (mode == 2 ? 128 : 0));
;     t.src = W + (size_t)mat * wstride + (size_t)k0 * N + n0; t.gain = gain ? gain + k0 : nullptr;
;     t.dst = (unsigned char*)WT + (size_t)mat * tstride_bytes + ((size_t)drow0 * K + k0) * esz; t.ldw = N; t.ldwt = K * esz; t.fp8 = fp8; t.scale = scale; return true;
; }
; __device__ __forceinline__ void titem_load(const TItem& t, f32x4 (&v)[2][8], f32x4 (&g)[2], int lane) {
;     const int n4 = lane & 7, kr = lane >> 3;
;     const float* gp = t.gain ? t.gain : t.src;
; #pragma unroll
;     for (int h = 0; h < 2; ++h)
; #pragma unroll
;         for (int i = 0; i < 8; ++i) v[h][i] = *(const f32x4*)(t.src + (size_t)(8 * kr + i) * t.ldw + 32 * h + 4 * n4);
;     g[0] = *(const f32x4*)(gp + 8 * kr); g[1] = *(const f32x4*)(gp + 8 * kr + 4);
; }
	s_waitcnt vmcnt(0)
	s_load_dwordx2 s[4:5], s[66:67], 0xd0
	s_load_dwordx2 s[8:9], s[66:67], 0xe0
	s_waitcnt lgkmcnt(0)
	s_add_u32 s8, s8, 0x27000000
	s_addc_u32 s9, s9, 0
	s_mov_b32 s35, 0
	s_lshl_b32 s37, s35, 11
	s_add_i32 s37, s37, s25
	s_lshr_b32 s45, s37, 9
	s_mul_i32 s45, s45, 0x2493
	s_lshr_b32 s45, s45, 16
	s_mul_i32 s51, s45, 0xe00
	s_sub_i32 s50, s37, s51
	s_lshr_b32 s51, s50, 5
	s_and_b32 s52, s50, 31
	s_mul_i32 s63, s45, 0x3800000
	s_add_u32 s46, s4, s63
	s_addc_u32 s47, s5, 0
	s_lshl_b32 s63, s51, 19
	s_lshl_b32 s37, s52, 8
	s_add_i32 s63, s63, s37
	s_add_u32 s46, s46, s63
	s_addc_u32 s47, s47, 0
	s_mov_b64 s[48:49], s[4:5]
	s_mul_i32 s63, s45, 0xe00000
	s_mul_i32 s37, s52, 0x70000
	s_add_i32 s63, s63, s37
	s_lshl_b32 s37, s51, 6
	s_add_i32 s63, s63, s37
	s_add_u32 s38, s8, s63
	s_addc_u32 s39, s9, 0
	global_load_dwordx4 v[0:3], v221, s[46:47]
	global_load_dwordx4 v[32:35], v221, s[46:47] offset:128
	v_add_u32_e32 v238, 0x2000, v221
	global_load_dwordx4 v[4:7], v238, s[46:47]
	global_load_dwordx4 v[36:39], v238, s[46:47] offset:128
	v_add_u32_e32 v238, 0x4000, v221
	global_load_dwordx4 v[8:11], v238, s[46:47]
	global_load_dwordx4 v[40:43], v238, s[46:47] offset:128
	v_add_u32_e32 v238, 0x6000, v221
	global_load_dwordx4 v[12:15], v238, s[46:47]
	global_load_dwordx4 v[44:47], v238, s[46:47] offset:128
	v_add_u32_e32 v238, 0x8000, v221
	global_load_dwordx4 v[16:19], v238, s[46:47]
	global_load_dwordx4 v[48:51], v238, s[46:47] offset:128
	v_add_u32_e32 v238, 0xa000, v221
	global_load_dwordx4 v[20:23], v238, s[46:47]
	global_load_dwordx4 v[52:55], v238, s[46:47] offset:128
	v_add_u32_e32 v238, 0xc000, v221
	global_load_dwordx4 v[24:27], v238, s[46:47]
	global_load_dwordx4 v[56:59], v238, s[46:47] offset:128
	v_add_u32_e32 v238, 0xe000, v221
	global_load_dwordx4 v[28:31], v238, s[46:47]
	global_load_dwordx4 v[60:63], v238, s[46:47] offset:128
	global_load_dwordx4 v[192:195], v222, s[48:49]
	global_load_dwordx4 v[196:199], v222, s[48:49] offset:16
	s_mov_b32 s35, 1
	s_lshl_b32 s37, s35, 11
	s_add_i32 s37, s37, s25
	s_lshr_b32 s45, s37, 9
	s_mul_i32 s45, s45, 0x2493
	s_lshr_b32 s45, s45, 16
	s_mul_i32 s51, s45, 0xe00
	s_sub_i32 s50, s37, s51
	s_lshr_b32 s51, s50, 5
	s_and_b32 s52, s50, 31
	s_mul_i32 s63, s45, 0x3800000
	s_add_u32 s46, s4, s63
	s_addc_u32 s47, s5, 0
	s_lshl_b32 s63, s51, 19
	s_lshl_b32 s37, s52, 8
	s_add_i32 s63, s63, s37
	s_add_u32 s46, s46, s63
	s_addc_u32 s47, s47, 0
	s_mov_b64 s[48:49], s[4:5]
	s_mul_i32 s63, s45, 0xe00000
	s_mul_i32 s37, s52, 0x70000
	s_add_i32 s63, s63, s37
	s_lshl_b32 s37, s51, 6
	s_add_i32 s63, s63, s37
	s_add_u32 s40, s8, s63
	s_addc_u32 s41, s9, 0
	global_load_dwordx4 v[64:67], v221, s[46:47]
	global_load_dwordx4 v[96:99], v221, s[46:47] offset:128
	v_add_u32_e32 v238, 0x2000, v221
	global_load_dwordx4 v[68:71], v238, s[46:47]
	global_load_dwordx4 v[100:103], v238, s[46:47] offset:128
	v_add_u32_e32 v238, 0x4000, v221
	global_load_dwordx4 v[72:75], v238, s[46:47]
	global_load_dwordx4 v[104:107], v238, s[46:47] offset:128
	v_add_u32_e32 v238, 0x6000, v221
	global_load_dwordx4 v[76:79], v238, s[46:47]
	global_load_dwordx4 v[108:111], v238, s[46:47] offset:128
	v_add_u32_e32 v238, 0x8000, v221
	global_load_dwordx4 v[80:83], v238, s[46:47]
	global_load_dwordx4 v[112:115], v238, s[46:47] offset:128
	v_add_u32_e32 v238, 0xa000, v221
	global_load_dwordx4 v[84:87], v238, s[46:47]
	global_load_dwordx4 v[116:119], v238, s[46:47] offset:128
	v_add_u32_e32 v238, 0xc000, v221
	global_load_dwordx4 v[88:91], v238, s[46:47]
	global_load_dwordx4 v[120:123], v238, s[46:47] offset:128
	v_add_u32_e32 v238, 0xe000, v221
	global_load_dwordx4 v[92:95], v238, s[46:47]
	global_load_dwordx4 v[124:127], v238, s[46:47] offset:128
	global_load_dwordx4 v[204:207], v222, s[48:49]
	global_load_dwordx4 v[208:211], v222, s[48:49] offset:16
	s_mov_b32 s35, 2
	s_lshl_b32 s37, s35, 11
	s_add_i32 s37, s37, s25
	s_lshr_b32 s45, s37, 9
	s_mul_i32 s45, s45, 0x2493
	s_lshr_b32 s45, s45, 16
	s_mul_i32 s51, s45, 0xe00
	s_sub_i32 s50, s37, s51
	s_lshr_b32 s51, s50, 5
	s_and_b32 s52, s50, 31
	s_mul_i32 s63, s45, 0x3800000
	s_add_u32 s46, s4, s63
	s_addc_u32 s47, s5, 0
	s_lshl_b32 s63, s51, 19
	s_lshl_b32 s37, s52, 8
	s_add_i32 s63, s63, s37
	s_add_u32 s46, s46, s63
	s_addc_u32 s47, s47, 0
	s_mov_b64 s[48:49], s[4:5]
	s_mul_i32 s63, s45, 0xe00000
	s_mul_i32 s37, s52, 0x70000
	s_add_i32 s63, s63, s37
	s_lshl_b32 s37, s51, 6
	s_add_i32 s63, s63, s37
	s_add_u32 s42, s8, s63
	s_addc_u32 s43, s9, 0
	global_load_dwordx4 v[128:131], v221, s[46:47]
	global_load_dwordx4 v[160:163], v221, s[46:47] offset:128
	v_add_u32_e32 v238, 0x2000, v221
	global_load_dwordx4 v[132:135], v238, s[46:47]
	global_load_dwordx4 v[164:167], v238, s[46:47] offset:128
	v_add_u32_e32 v238, 0x4000, v221
	global_load_dwordx4 v[136:139], v238, s[46:47]
	global_load_dwordx4 v[168:171], v238, s[46:47] offset:128
	v_add_u32_e32 v238, 0x6000, v221
	global_load_dwordx4 v[140:143], v238, s[46:47]
	global_load_dwordx4 v[172:175], v238, s[46:47] offset:128
	v_add_u32_e32 v238, 0x8000, v221
	global_load_dwordx4 v[144:147], v238, s[46:47]
	global_load_dwordx4 v[176:179], v238, s[46:47] offset:128
	v_add_u32_e32 v238, 0xa000, v221
	global_load_dwordx4 v[148:151], v238, s[46:47]
	global_load_dwordx4 v[180:183], v238, s[46:47] offset:128
	v_add_u32_e32 v238, 0xc000, v221
	global_load_dwordx4 v[152:155], v238, s[46:47]
	global_load_dwordx4 v[184:187], v238, s[46:47] offset:128
	v_add_u32_e32 v238, 0xe000, v221
	global_load_dwordx4 v[156:159], v238, s[46:47]
	global_load_dwordx4 v[188:191], v238, s[46:47] offset:128
	global_load_dwordx4 v[212:215], v222, s[48:49]
	global_load_dwordx4 v[216:219], v222, s[48:49] offset:16
	s_waitcnt vmcnt(36)
; __device__ __forceinline__ unsigned pk4_fp8(float a, float b, float c, float d) {
;     a = __builtin_amdgcn_fmed3f(a, -448.f, 448.f); b = __builtin_amdgcn_fmed3f(b, -448.f, 448.f); c = __builtin_amdgcn_fmed3f(c, -448.f, 448.f); d = __builtin_amdgcn_fmed3f(d, -448.f, 448.f);
;     unsigned w = 0u; w = __builtin_amdgcn_cvt_pk_fp8_f32(a, b, w, false); w = __builtin_amdgcn_cvt_pk_fp8_f32(c, d, w, true); return w;
; }
; __device__ __forceinline__ void titem_process(const TItem& t, const f32x4 (&v)[2][8], const f32x4 (&g)[2], int lane) {
;     const int n4 = lane & 7, kr = lane >> 3;
;     float s[8];
; #pragma unroll
;     for (int j = 0; j < 8; ++j) s[j] = t.gain ? g[j >> 2][j & 3] * t.scale : t.scale;
;     if (t.fp8 == 1) {
; #pragma unroll
;         for (int h = 0; h < 2; ++h)
; #pragma unroll
;             for (int i = 0; i < 4; ++i) { u32x2 o; o.x = epi::pk4_fp8(v[h][0][i] * s[0], v[h][1][i] * s[1], v[h][2][i] * s[2], v[h][3][i] * s[3]); o.y = epi::pk4_fp8(v[h][4][i] * s[4], v[h][5][i] * s[5], v[h][6][i] * s[6], v[h][7][i] * s[7]);
;                 __builtin_nontemporal_store(o, (u32x2*)(t.dst + (size_t)(32 * h + 4 * n4 + i) * t.ldwt + 8 * kr)); }
	v_mov_b32_e32 v226, 0x44000000
	v_mov_b32_e32 v227, 0x44000000
	v_mov_b32_e32 v228, 0x44000000
	v_mov_b32_e32 v229, 0x44000000
	v_mov_b32_e32 v230, 0x44000000
	v_mov_b32_e32 v231, 0x44000000
	v_mov_b32_e32 v232, 0x44000000
	v_mov_b32_e32 v233, 0x44000000
	v_pk_mul_f32 v[0:1], v[0:1], v[226:227] op_sel:[0,0] op_sel_hi:[1,0]
	v_pk_mul_f32 v[4:5], v[4:5], v[226:227] op_sel:[0,1] op_sel_hi:[1,1]
	v_pk_mul_f32 v[8:9], v[8:9], v[228:229] op_sel:[0,0] op_sel_hi:[1,0]
	v_pk_mul_f32 v[12:13], v[12:13], v[228:229] op_sel:[0,1] op_sel_hi:[1,1]
	v_pk_mul_f32 v[16:17], v[16:17], v[230:231] op_sel:[0,0] op_sel_hi:[1,0]
	v_pk_mul_f32 v[20:21], v[20:21], v[230:231] op_sel:[0,1] op_sel_hi:[1,1]
	v_pk_mul_f32 v[24:25], v[24:25], v[232:233] op_sel:[0,0] op_sel_hi:[1,0]
	v_pk_mul_f32 v[28:29], v[28:29], v[232:233] op_sel:[0,1] op_sel_hi:[1,1]
	v_pk_mul_f32 v[2:3], v[2:3], v[226:227] op_sel:[0,0] op_sel_hi:[1,0]
	v_pk_mul_f32 v[6:7], v[6:7], v[226:227] op_sel:[0,1] op_sel_hi:[1,1]
	v_pk_mul_f32 v[10:11], v[10:11], v[228:229] op_sel:[0,0] op_sel_hi:[1,0]
	v_pk_mul_f32 v[14:15], v[14:15], v[228:229] op_sel:[0,1] op_sel_hi:[1,1]
	v_pk_mul_f32 v[18:19], v[18:19], v[230:231] op_sel:[0,0] op_sel_hi:[1,0]
	v_pk_mul_f32 v[22:23], v[22:23], v[230:231] op_sel:[0,1] op_sel_hi:[1,1]
	v_pk_mul_f32 v[26:27], v[26:27], v[232:233] op_sel:[0,0] op_sel_hi:[1,0]
	v_pk_mul_f32 v[30:31], v[30:31], v[232:233] op_sel:[0,1] op_sel_hi:[1,1]
	v_pk_mul_f32 v[32:33], v[32:33], v[226:227] op_sel:[0,0] op_sel_hi:[1,0]
	v_pk_mul_f32 v[36:37], v[36:37], v[226:227] op_sel:[0,1] op_sel_hi:[1,1]
	v_pk_mul_f32 v[40:41], v[40:41], v[228:229] op_sel:[0,0] op_sel_hi:[1,0]
	v_pk_mul_f32 v[44:45], v[44:45], v[228:229] op_sel:[0,1] op_sel_hi:[1,1]
	v_pk_mul_f32 v[48:49], v[48:49], v[230:231] op_sel:[0,0] op_sel_hi:[1,0]
	v_pk_mul_f32 v[52:53], v[52:53], v[230:231] op_sel:[0,1] op_sel_hi:[1,1]
	v_pk_mul_f32 v[56:57], v[56:57], v[232:233] op_sel:[0,0] op_sel_hi:[1,0]
	v_pk_mul_f32 v[60:61], v[60:61], v[232:233] op_sel:[0,1] op_sel_hi:[1,1]
	v_pk_mul_f32 v[34:35], v[34:35], v[226:227] op_sel:[0,0] op_sel_hi:[1,0]
	v_pk_mul_f32 v[38:39], v[38:39], v[226:227] op_sel:[0,1] op_sel_hi:[1,1]
	v_pk_mul_f32 v[42:43], v[42:43], v[228:229] op_sel:[0,0] op_sel_hi:[1,0]
	v_pk_mul_f32 v[46:47], v[46:47], v[228:229] op_sel:[0,1] op_sel_hi:[1,1]
	v_pk_mul_f32 v[50:51], v[50:51], v[230:231] op_sel:[0,0] op_sel_hi:[1,0]
	v_pk_mul_f32 v[54:55], v[54:55], v[230:231] op_sel:[0,1] op_sel_hi:[1,1]
	v_pk_mul_f32 v[58:59], v[58:59], v[232:233] op_sel:[0,0] op_sel_hi:[1,0]
	v_pk_mul_f32 v[62:63], v[62:63], v[232:233] op_sel:[0,1] op_sel_hi:[1,1]
	v_med3_f32 v0, v0, s33, v225
	v_med3_f32 v1, v1, s33, v225
	v_med3_f32 v2, v2, s33, v225
	v_med3_f32 v3, v3, s33, v225
	v_med3_f32 v4, v4, s33, v225
	v_med3_f32 v5, v5, s33, v225
	v_med3_f32 v6, v6, s33, v225
	v_med3_f32 v7, v7, s33, v225
	v_med3_f32 v8, v8, s33, v225
	v_med3_f32 v9, v9, s33, v225
	v_med3_f32 v10, v10, s33, v225
	v_med3_f32 v11, v11, s33, v225
	v_med3_f32 v12, v12, s33, v225
	v_med3_f32 v13, v13, s33, v225
	v_med3_f32 v14, v14, s33, v225
	v_med3_f32 v15, v15, s33, v225
	v_med3_f32 v16, v16, s33, v225
	v_med3_f32 v17, v17, s33, v225
	v_med3_f32 v18, v18, s33, v225
	v_med3_f32 v19, v19, s33, v225
	v_med3_f32 v20, v20, s33, v225
	v_med3_f32 v21, v21, s33, v225
	v_med3_f32 v22, v22, s33, v225
	v_med3_f32 v23, v23, s33, v225
	v_med3_f32 v24, v24, s33, v225
	v_med3_f32 v25, v25, s33, v225
	v_med3_f32 v26, v26, s33, v225
	v_med3_f32 v27, v27, s33, v225
	v_med3_f32 v28, v28, s33, v225
	v_med3_f32 v29, v29, s33, v225
	v_med3_f32 v30, v30, s33, v225
	v_med3_f32 v31, v31, s33, v225
	v_med3_f32 v32, v32, s33, v225
	v_med3_f32 v33, v33, s33, v225
	v_med3_f32 v34, v34, s33, v225
	v_med3_f32 v35, v35, s33, v225
	v_med3_f32 v36, v36, s33, v225
	v_med3_f32 v37, v37, s33, v225
	v_med3_f32 v38, v38, s33, v225
	v_med3_f32 v39, v39, s33, v225
	v_med3_f32 v40, v40, s33, v225
	v_med3_f32 v41, v41, s33, v225
	v_med3_f32 v42, v42, s33, v225
	v_med3_f32 v43, v43, s33, v225
	v_med3_f32 v44, v44, s33, v225
	v_med3_f32 v45, v45, s33, v225
	v_med3_f32 v46, v46, s33, v225
	v_med3_f32 v47, v47, s33, v225
	v_med3_f32 v48, v48, s33, v225
	v_med3_f32 v49, v49, s33, v225
	v_med3_f32 v50, v50, s33, v225
	v_med3_f32 v51, v51, s33, v225
	v_med3_f32 v52, v52, s33, v225
	v_med3_f32 v53, v53, s33, v225
	v_med3_f32 v54, v54, s33, v225
	v_med3_f32 v55, v55, s33, v225
	v_med3_f32 v56, v56, s33, v225
	v_med3_f32 v57, v57, s33, v225
	v_med3_f32 v58, v58, s33, v225
	v_med3_f32 v59, v59, s33, v225
	v_med3_f32 v60, v60, s33, v225
	v_med3_f32 v61, v61, s33, v225
	v_med3_f32 v62, v62, s33, v225
	v_med3_f32 v63, v63, s33, v225
	v_cvt_pk_fp8_f32 v234, v0, v4
	v_cvt_pk_fp8_f32 v235, v16, v20
	v_cvt_pk_fp8_f32 v234, v8, v12 op_sel:[0,0,1]
	v_cvt_pk_fp8_f32 v235, v24, v28 op_sel:[0,0,1]
	s_nop 0
	global_store_dwordx2 v224, v[234:235], s[38:39] nt
	v_cvt_pk_fp8_f32 v236, v1, v5
	v_cvt_pk_fp8_f32 v237, v17, v21
	v_cvt_pk_fp8_f32 v236, v9, v13 op_sel:[0,0,1]
	v_cvt_pk_fp8_f32 v237, v25, v29 op_sel:[0,0,1]
	v_add_u32_e32 v238, 0x1c00, v224
	global_store_dwordx2 v238, v[236:237], s[38:39] nt
	v_cvt_pk_fp8_f32 v234, v2, v6
	v_cvt_pk_fp8_f32 v235, v18, v22
	v_cvt_pk_fp8_f32 v234, v10, v14 op_sel:[0,0,1]
	v_cvt_pk_fp8_f32 v235, v26, v30 op_sel:[0,0,1]
	v_add_u32_e32 v238, 0x3800, v224
	global_store_dwordx2 v238, v[234:235], s[38:39] nt
	v_cvt_pk_fp8_f32 v236, v3, v7
	v_cvt_pk_fp8_f32 v237, v19, v23
	v_cvt_pk_fp8_f32 v236, v11, v15 op_sel:[0,0,1]
	v_cvt_pk_fp8_f32 v237, v27, v31 op_sel:[0,0,1]
	v_add_u32_e32 v238, 0x5400, v224
	global_store_dwordx2 v238, v[236:237], s[38:39] nt
	v_cvt_pk_fp8_f32 v234, v32, v36
	v_cvt_pk_fp8_f32 v235, v48, v52
	v_cvt_pk_fp8_f32 v234, v40, v44 op_sel:[0,0,1]
	v_cvt_pk_fp8_f32 v235, v56, v60 op_sel:[0,0,1]
	v_add_u32_e32 v238, 0x38000, v224
	global_store_dwordx2 v238, v[234:235], s[38:39] nt
	v_cvt_pk_fp8_f32 v236, v33, v37
	v_cvt_pk_fp8_f32 v237, v49, v53
	v_cvt_pk_fp8_f32 v236, v41, v45 op_sel:[0,0,1]
	v_cvt_pk_fp8_f32 v237, v57, v61 op_sel:[0,0,1]
	v_add_u32_e32 v238, 0x39c00, v224
	global_store_dwordx2 v238, v[236:237], s[38:39] nt
	v_cvt_pk_fp8_f32 v234, v34, v38
	v_cvt_pk_fp8_f32 v235, v50, v54
	v_cvt_pk_fp8_f32 v234, v42, v46 op_sel:[0,0,1]
	v_cvt_pk_fp8_f32 v235, v58, v62 op_sel:[0,0,1]
	v_add_u32_e32 v238, 0x3b800, v224
	global_store_dwordx2 v238, v[234:235], s[38:39] nt
	v_cvt_pk_fp8_f32 v236, v35, v39
	v_cvt_pk_fp8_f32 v237, v51, v55
	v_cvt_pk_fp8_f32 v236, v43, v47 op_sel:[0,0,1]
	v_cvt_pk_fp8_f32 v237, v59, v63 op_sel:[0,0,1]
	v_add_u32_e32 v238, 0x3d400, v224
	global_store_dwordx2 v238, v[236:237], s[38:39] nt
	s_mov_b32 s27, 1
	s_mov_b32 s30, 5
; __device__ __forceinline__ bool titem_group(int& it, TItem& t, const float* W, size_t wstride, int nmat, int K, int N, const float* gain, float scale, void* WT, size_t tstride_bytes, int mode, int fp8) {
;     const int nblk = N / 64, per = (K / 64) * nblk, tot = per * nmat;
;     if (it >= tot) { it -= tot; return false; }
;     const int mat = it / per, r = it % per, k0 = 64 * (r / nblk), n0 = 64 * (r % nblk), esz = (fp8 == 1) ? 1 : 2;
;     const int drow0 = (mode == 0) ? n0 : (256 * (n0 / 128) + (n0 % 128) + (mode == 2 ? 128 : 0));
;     t.src = W + (size_t)mat * wstride + (size_t)k0 * N + n0; t.gain = gain ? gain + k0 : nullptr;
;     t.dst = (unsigned char*)WT + (size_t)mat * tstride_bytes + ((size_t)drow0 * K + k0) * esz; t.ldw = N; t.ldwt = K * esz; t.fp8 = fp8; t.scale = scale; return true;
; }
; __device__ __forceinline__ void titem_load(const TItem& t, f32x4 (&v)[2][8], f32x4 (&g)[2], int lane) {
;     const int n4 = lane & 7, kr = lane >> 3;
;     const float* gp = t.gain ? t.gain : t.src;
; #pragma unroll
;     for (int h = 0; h < 2; ++h)
; #pragma unroll
;         for (int i = 0; i < 8; ++i) v[h][i] = *(const f32x4*)(t.src + (size_t)(8 * kr + i) * t.ldw + 32 * h + 4 * n4);
;     g[0] = *(const f32x4*)(gp + 8 * kr); g[1] = *(const f32x4*)(gp + 8 * kr + 4);
; }
; __device__ __forceinline__ void titem_process(const TItem& t, const f32x4 (&v)[2][8], const f32x4 (&g)[2], int lane) {
;     const int n4 = lane & 7, kr = lane >> 3;
;     float s[8];
; #pragma unroll
;     for (int j = 0; j < 8; ++j) s[j] = t.gain ? g[j >> 2][j & 3] * t.scale : t.scale;
;     if (t.fp8 == 1) {
; #pragma unroll
;         for (int h = 0; h < 2; ++h)
; #pragma unroll
;             for (int i = 0; i < 4; ++i) { u32x2 o; o.x = epi::pk4_fp8(v[h][0][i] * s[0], v[h][1][i] * s[1], v[h][2][i] * s[2], v[h][3][i] * s[3]); o.y = epi::pk4_fp8(v[h][4][i] * s[4], v[h][5][i] * s[5], v[h][6][i] * s[6], v[h][7][i] * s[7]);
;                 __builtin_nontemporal_store(o, (u32x2*)(t.dst + (size_t)(32 * h + 4 * n4 + i) * t.ldwt + 8 * kr)); }
.Lcv1_dn:
	s_add_i32 s35, s27, 2
	s_min_u32 s35, s35, 13
	s_lshl_b32 s37, s35, 11
	s_add_i32 s37, s37, s25
	s_lshr_b32 s45, s37, 9
	s_mul_i32 s45, s45, 0x2493
	s_lshr_b32 s45, s45, 16
	s_mul_i32 s51, s45, 0xe00
	s_sub_i32 s50, s37, s51
	s_lshr_b32 s51, s50, 5
	s_and_b32 s52, s50, 31
	s_mul_i32 s63, s45, 0x3800000
	s_add_u32 s46, s4, s63
	s_addc_u32 s47, s5, 0
	s_lshl_b32 s63, s51, 19
	s_lshl_b32 s37, s52, 8
	s_add_i32 s63, s63, s37
	s_add_u32 s46, s46, s63
	s_addc_u32 s47, s47, 0
	s_mov_b64 s[48:49], s[4:5]
	s_mul_i32 s63, s45, 0xe00000
	s_mul_i32 s37, s52, 0x70000
	s_add_i32 s63, s63, s37
	s_lshl_b32 s37, s51, 6
	s_add_i32 s63, s63, s37
	s_add_u32 s38, s8, s63
	s_addc_u32 s39, s9, 0
	global_load_dwordx4 v[0:3], v221, s[46:47]
	global_load_dwordx4 v[32:35], v221, s[46:47] offset:128
	v_add_u32_e32 v238, 0x2000, v221
	global_load_dwordx4 v[4:7], v238, s[46:47]
	global_load_dwordx4 v[36:39], v238, s[46:47] offset:128
	v_add_u32_e32 v238, 0x4000, v221
	global_load_dwordx4 v[8:11], v238, s[46:47]
	global_load_dwordx4 v[40:43], v238, s[46:47] offset:128
	v_add_u32_e32 v238, 0x6000, v221
	global_load_dwordx4 v[12:15], v238, s[46:47]
	global_load_dwordx4 v[44:47], v238, s[46:47] offset:128
	v_add_u32_e32 v238, 0x8000, v221
	global_load_dwordx4 v[16:19], v238, s[46:47]
	global_load_dwordx4 v[48:51], v238, s[46:47] offset:128
	v_add_u32_e32 v238, 0xa000, v221
	global_load_dwordx4 v[20:23], v238, s[46:47]
	global_load_dwordx4 v[52:55], v238, s[46:47] offset:128
	v_add_u32_e32 v238, 0xc000, v221
	global_load_dwordx4 v[24:27], v238, s[46:47]
	global_load_dwordx4 v[56:59], v238, s[46:47] offset:128
	v_add_u32_e32 v238, 0xe000, v221
	global_load_dwordx4 v[28:31], v238, s[46:47]
	global_load_dwordx4 v[60:63], v238, s[46:47] offset:128
	global_load_dwordx4 v[192:195], v222, s[48:49]
	global_load_dwordx4 v[196:199], v222, s[48:49] offset:16
	s_waitcnt vmcnt(44)
	v_mov_b32_e32 v226, 0x44000000
	v_mov_b32_e32 v227, 0x44000000
	v_mov_b32_e32 v228, 0x44000000
	v_mov_b32_e32 v229, 0x44000000
	v_mov_b32_e32 v230, 0x44000000
	v_mov_b32_e32 v231, 0x44000000
	v_mov_b32_e32 v232, 0x44000000
	v_mov_b32_e32 v233, 0x44000000
	v_pk_mul_f32 v[64:65], v[64:65], v[226:227] op_sel:[0,0] op_sel_hi:[1,0]
	v_pk_mul_f32 v[68:69], v[68:69], v[226:227] op_sel:[0,1] op_sel_hi:[1,1]
	v_pk_mul_f32 v[72:73], v[72:73], v[228:229] op_sel:[0,0] op_sel_hi:[1,0]
	v_pk_mul_f32 v[76:77], v[76:77], v[228:229] op_sel:[0,1] op_sel_hi:[1,1]
	v_pk_mul_f32 v[80:81], v[80:81], v[230:231] op_sel:[0,0] op_sel_hi:[1,0]
	v_pk_mul_f32 v[84:85], v[84:85], v[230:231] op_sel:[0,1] op_sel_hi:[1,1]
	v_pk_mul_f32 v[88:89], v[88:89], v[232:233] op_sel:[0,0] op_sel_hi:[1,0]
	v_pk_mul_f32 v[92:93], v[92:93], v[232:233] op_sel:[0,1] op_sel_hi:[1,1]
	v_pk_mul_f32 v[66:67], v[66:67], v[226:227] op_sel:[0,0] op_sel_hi:[1,0]
	v_pk_mul_f32 v[70:71], v[70:71], v[226:227] op_sel:[0,1] op_sel_hi:[1,1]
	v_pk_mul_f32 v[74:75], v[74:75], v[228:229] op_sel:[0,0] op_sel_hi:[1,0]
	v_pk_mul_f32 v[78:79], v[78:79], v[228:229] op_sel:[0,1] op_sel_hi:[1,1]
	v_pk_mul_f32 v[82:83], v[82:83], v[230:231] op_sel:[0,0] op_sel_hi:[1,0]
	v_pk_mul_f32 v[86:87], v[86:87], v[230:231] op_sel:[0,1] op_sel_hi:[1,1]
	v_pk_mul_f32 v[90:91], v[90:91], v[232:233] op_sel:[0,0] op_sel_hi:[1,0]
	v_pk_mul_f32 v[94:95], v[94:95], v[232:233] op_sel:[0,1] op_sel_hi:[1,1]
	v_pk_mul_f32 v[96:97], v[96:97], v[226:227] op_sel:[0,0] op_sel_hi:[1,0]
	v_pk_mul_f32 v[100:101], v[100:101], v[226:227] op_sel:[0,1] op_sel_hi:[1,1]
	v_pk_mul_f32 v[104:105], v[104:105], v[228:229] op_sel:[0,0] op_sel_hi:[1,0]
	v_pk_mul_f32 v[108:109], v[108:109], v[228:229] op_sel:[0,1] op_sel_hi:[1,1]
	v_pk_mul_f32 v[112:113], v[112:113], v[230:231] op_sel:[0,0] op_sel_hi:[1,0]
	v_pk_mul_f32 v[116:117], v[116:117], v[230:231] op_sel:[0,1] op_sel_hi:[1,1]
	v_pk_mul_f32 v[120:121], v[120:121], v[232:233] op_sel:[0,0] op_sel_hi:[1,0]
	v_pk_mul_f32 v[124:125], v[124:125], v[232:233] op_sel:[0,1] op_sel_hi:[1,1]
	v_pk_mul_f32 v[98:99], v[98:99], v[226:227] op_sel:[0,0] op_sel_hi:[1,0]
	v_pk_mul_f32 v[102:103], v[102:103], v[226:227] op_sel:[0,1] op_sel_hi:[1,1]
	v_pk_mul_f32 v[106:107], v[106:107], v[228:229] op_sel:[0,0] op_sel_hi:[1,0]
	v_pk_mul_f32 v[110:111], v[110:111], v[228:229] op_sel:[0,1] op_sel_hi:[1,1]
	v_pk_mul_f32 v[114:115], v[114:115], v[230:231] op_sel:[0,0] op_sel_hi:[1,0]
	v_pk_mul_f32 v[118:119], v[118:119], v[230:231] op_sel:[0,1] op_sel_hi:[1,1]
	v_pk_mul_f32 v[122:123], v[122:123], v[232:233] op_sel:[0,0] op_sel_hi:[1,0]
	v_pk_mul_f32 v[126:127], v[126:127], v[232:233] op_sel:[0,1] op_sel_hi:[1,1]
	v_med3_f32 v64, v64, s33, v225
	v_med3_f32 v65, v65, s33, v225
	v_med3_f32 v66, v66, s33, v225
	v_med3_f32 v67, v67, s33, v225
	v_med3_f32 v68, v68, s33, v225
	v_med3_f32 v69, v69, s33, v225
	v_med3_f32 v70, v70, s33, v225
	v_med3_f32 v71, v71, s33, v225
	v_med3_f32 v72, v72, s33, v225
	v_med3_f32 v73, v73, s33, v225
	v_med3_f32 v74, v74, s33, v225
	v_med3_f32 v75, v75, s33, v225
	v_med3_f32 v76, v76, s33, v225
	v_med3_f32 v77, v77, s33, v225
	v_med3_f32 v78, v78, s33, v225
	v_med3_f32 v79, v79, s33, v225
	v_med3_f32 v80, v80, s33, v225
	v_med3_f32 v81, v81, s33, v225
	v_med3_f32 v82, v82, s33, v225
	v_med3_f32 v83, v83, s33, v225
	v_med3_f32 v84, v84, s33, v225
	v_med3_f32 v85, v85, s33, v225
	v_med3_f32 v86, v86, s33, v225
	v_med3_f32 v87, v87, s33, v225
	v_med3_f32 v88, v88, s33, v225
	v_med3_f32 v89, v89, s33, v225
	v_med3_f32 v90, v90, s33, v225
	v_med3_f32 v91, v91, s33, v225
	v_med3_f32 v92, v92, s33, v225
	v_med3_f32 v93, v93, s33, v225
	v_med3_f32 v94, v94, s33, v225
	v_med3_f32 v95, v95, s33, v225
	v_med3_f32 v96, v96, s33, v225
	v_med3_f32 v97, v97, s33, v225
; __device__ __forceinline__ bool titem_group(int& it, TItem& t, const float* W, size_t wstride, int nmat, int K, int N, const float* gain, float scale, void* WT, size_t tstride_bytes, int mode, int fp8) {
;     const int nblk = N / 64, per = (K / 64) * nblk, tot = per * nmat;
;     if (it >= tot) { it -= tot; return false; }
;     const int mat = it / per, r = it % per, k0 = 64 * (r / nblk), n0 = 64 * (r % nblk), esz = (fp8 == 1) ? 1 : 2;
;     const int drow0 = (mode == 0) ? n0 : (256 * (n0 / 128) + (n0 % 128) + (mode == 2 ? 128 : 0));
;     t.src = W + (size_t)mat * wstride + (size_t)k0 * N + n0; t.gain = gain ? gain + k0 : nullptr;
;     t.dst = (unsigned char*)WT + (size_t)mat * tstride_bytes + ((size_t)drow0 * K + k0) * esz; t.ldw = N; t.ldwt = K * esz; t.fp8 = fp8; t.scale = scale; return true;
; }
; __device__ __forceinline__ void titem_load(const TItem& t, f32x4 (&v)[2][8], f32x4 (&g)[2], int lane) {
;     const int n4 = lane & 7, kr = lane >> 3;
;     const float* gp = t.gain ? t.gain : t.src;
; #pragma unroll
;     for (int h = 0; h < 2; ++h)
; #pragma unroll
;         for (int i = 0; i < 8; ++i) v[h][i] = *(const f32x4*)(t.src + (size_t)(8 * kr + i) * t.ldw + 32 * h + 4 * n4);
;     g[0] = *(const f32x4*)(gp + 8 * kr); g[1] = *(const f32x4*)(gp + 8 * kr + 4);
; }
; __device__ __forceinline__ void titem_process(const TItem& t, const f32x4 (&v)[2][8], const f32x4 (&g)[2], int lane) {
;     const int n4 = lane & 7, kr = lane >> 3;
;     float s[8];
; #pragma unroll
;     for (int j = 0; j < 8; ++j) s[j] = t.gain ? g[j >> 2][j & 3] * t.scale : t.scale;
;     if (t.fp8 == 1) {
; #pragma unroll
;         for (int h = 0; h < 2; ++h)
; #pragma unroll
;             for (int i = 0; i < 4; ++i) { u32x2 o; o.x = epi::pk4_fp8(v[h][0][i] * s[0], v[h][1][i] * s[1], v[h][2][i] * s[2], v[h][3][i] * s[3]); o.y = epi::pk4_fp8(v[h][4][i] * s[4], v[h][5][i] * s[5], v[h][6][i] * s[6], v[h][7][i] * s[7]);
;                 __builtin_nontemporal_store(o, (u32x2*)(t.dst + (size_t)(32 * h + 4 * n4 + i) * t.ldwt + 8 * kr)); }
	v_med3_f32 v98, v98, s33, v225
	v_med3_f32 v99, v99, s33, v225
	v_med3_f32 v100, v100, s33, v225
	v_med3_f32 v101, v101, s33, v225
	v_med3_f32 v102, v102, s33, v225
	v_med3_f32 v103, v103, s33, v225
	v_med3_f32 v104, v104, s33, v225
	v_med3_f32 v105, v105, s33, v225
	v_med3_f32 v106, v106, s33, v225
	v_med3_f32 v107, v107, s33, v225
	v_med3_f32 v108, v108, s33, v225
	v_med3_f32 v109, v109, s33, v225
	v_med3_f32 v110, v110, s33, v225
	v_med3_f32 v111, v111, s33, v225
	v_med3_f32 v112, v112, s33, v225
	v_med3_f32 v113, v113, s33, v225
	v_med3_f32 v114, v114, s33, v225
	v_med3_f32 v115, v115, s33, v225
	v_med3_f32 v116, v116, s33, v225
	v_med3_f32 v117, v117, s33, v225
	v_med3_f32 v118, v118, s33, v225
	v_med3_f32 v119, v119, s33, v225
	v_med3_f32 v120, v120, s33, v225
	v_med3_f32 v121, v121, s33, v225
	v_med3_f32 v122, v122, s33, v225
	v_med3_f32 v123, v123, s33, v225
	v_med3_f32 v124, v124, s33, v225
	v_med3_f32 v125, v125, s33, v225
	v_med3_f32 v126, v126, s33, v225
	v_med3_f32 v127, v127, s33, v225
	v_cvt_pk_fp8_f32 v234, v64, v68
	v_cvt_pk_fp8_f32 v235, v80, v84
	v_cvt_pk_fp8_f32 v234, v72, v76 op_sel:[0,0,1]
	v_cvt_pk_fp8_f32 v235, v88, v92 op_sel:[0,0,1]
	s_nop 0
	global_store_dwordx2 v224, v[234:235], s[40:41] nt
	v_cvt_pk_fp8_f32 v236, v65, v69
	v_cvt_pk_fp8_f32 v237, v81, v85
	v_cvt_pk_fp8_f32 v236, v73, v77 op_sel:[0,0,1]
	v_cvt_pk_fp8_f32 v237, v89, v93 op_sel:[0,0,1]
	v_add_u32_e32 v238, 0x1c00, v224
	global_store_dwordx2 v238, v[236:237], s[40:41] nt
	v_cvt_pk_fp8_f32 v234, v66, v70
	v_cvt_pk_fp8_f32 v235, v82, v86
	v_cvt_pk_fp8_f32 v234, v74, v78 op_sel:[0,0,1]
	v_cvt_pk_fp8_f32 v235, v90, v94 op_sel:[0,0,1]
	v_add_u32_e32 v238, 0x3800, v224
	global_store_dwordx2 v238, v[234:235], s[40:41] nt
	v_cvt_pk_fp8_f32 v236, v67, v71
	v_cvt_pk_fp8_f32 v237, v83, v87
	v_cvt_pk_fp8_f32 v236, v75, v79 op_sel:[0,0,1]
	v_cvt_pk_fp8_f32 v237, v91, v95 op_sel:[0,0,1]
	v_add_u32_e32 v238, 0x5400, v224
	global_store_dwordx2 v238, v[236:237], s[40:41] nt
	v_cvt_pk_fp8_f32 v234, v96, v100
	v_cvt_pk_fp8_f32 v235, v112, v116
	v_cvt_pk_fp8_f32 v234, v104, v108 op_sel:[0,0,1]
	v_cvt_pk_fp8_f32 v235, v120, v124 op_sel:[0,0,1]
	v_add_u32_e32 v238, 0x38000, v224
	global_store_dwordx2 v238, v[234:235], s[40:41] nt
	v_cvt_pk_fp8_f32 v236, v97, v101
	v_cvt_pk_fp8_f32 v237, v113, v117
	v_cvt_pk_fp8_f32 v236, v105, v109 op_sel:[0,0,1]
	v_cvt_pk_fp8_f32 v237, v121, v125 op_sel:[0,0,1]
	v_add_u32_e32 v238, 0x39c00, v224
	global_store_dwordx2 v238, v[236:237], s[40:41] nt
	v_cvt_pk_fp8_f32 v234, v98, v102
	v_cvt_pk_fp8_f32 v235, v114, v118
	v_cvt_pk_fp8_f32 v234, v106, v110 op_sel:[0,0,1]
	v_cvt_pk_fp8_f32 v235, v122, v126 op_sel:[0,0,1]
	v_add_u32_e32 v238, 0x3b800, v224
	global_store_dwordx2 v238, v[234:235], s[40:41] nt
	v_cvt_pk_fp8_f32 v236, v99, v103
	v_cvt_pk_fp8_f32 v237, v115, v119
	v_cvt_pk_fp8_f32 v236, v107, v111 op_sel:[0,0,1]
	v_cvt_pk_fp8_f32 v237, v123, v127 op_sel:[0,0,1]
	v_add_u32_e32 v238, 0x3d400, v224
	global_store_dwordx2 v238, v[236:237], s[40:41] nt
	s_add_i32 s35, s27, 3
	s_min_u32 s35, s35, 13
	s_lshl_b32 s37, s35, 11
	s_add_i32 s37, s37, s25
	s_lshr_b32 s45, s37, 9
	s_mul_i32 s45, s45, 0x2493
	s_lshr_b32 s45, s45, 16
	s_mul_i32 s51, s45, 0xe00
	s_sub_i32 s50, s37, s51
	s_lshr_b32 s51, s50, 5
	s_and_b32 s52, s50, 31
	s_mul_i32 s63, s45, 0x3800000
	s_add_u32 s46, s4, s63
	s_addc_u32 s47, s5, 0
	s_lshl_b32 s63, s51, 19
	s_lshl_b32 s37, s52, 8
	s_add_i32 s63, s63, s37
	s_add_u32 s46, s46, s63
	s_addc_u32 s47, s47, 0
	s_mov_b64 s[48:49], s[4:5]
	s_mul_i32 s63, s45, 0xe00000
	s_mul_i32 s37, s52, 0x70000
	s_add_i32 s63, s63, s37
	s_lshl_b32 s37, s51, 6
	s_add_i32 s63, s63, s37
	s_add_u32 s40, s8, s63
	s_addc_u32 s41, s9, 0
	global_load_dwordx4 v[64:67], v221, s[46:47]
	global_load_dwordx4 v[96:99], v221, s[46:47] offset:128
	v_add_u32_e32 v238, 0x2000, v221
	global_load_dwordx4 v[68:71], v238, s[46:47]
	global_load_dwordx4 v[100:103], v238, s[46:47] offset:128
	v_add_u32_e32 v238, 0x4000, v221
	global_load_dwordx4 v[72:75], v238, s[46:47]
	global_load_dwordx4 v[104:107], v238, s[46:47] offset:128
	v_add_u32_e32 v238, 0x6000, v221
	global_load_dwordx4 v[76:79], v238, s[46:47]
	global_load_dwordx4 v[108:111], v238, s[46:47] offset:128
	v_add_u32_e32 v238, 0x8000, v221
	global_load_dwordx4 v[80:83], v238, s[46:47]
	global_load_dwordx4 v[112:115], v238, s[46:47] offset:128
	v_add_u32_e32 v238, 0xa000, v221
	global_load_dwordx4 v[84:87], v238, s[46:47]
	global_load_dwordx4 v[116:119], v238, s[46:47] offset:128
	v_add_u32_e32 v238, 0xc000, v221
	global_load_dwordx4 v[88:91], v238, s[46:47]
	global_load_dwordx4 v[120:123], v238, s[46:47] offset:128
	v_add_u32_e32 v238, 0xe000, v221
	global_load_dwordx4 v[92:95], v238, s[46:47]
	global_load_dwordx4 v[124:127], v238, s[46:47] offset:128
	global_load_dwordx4 v[204:207], v222, s[48:49]
	global_load_dwordx4 v[208:211], v222, s[48:49] offset:16
	s_waitcnt vmcnt(44)
; __device__ __forceinline__ unsigned pk4_fp8(float a, float b, float c, float d) {
;     a = __builtin_amdgcn_fmed3f(a, -448.f, 448.f); b = __builtin_amdgcn_fmed3f(b, -448.f, 448.f); c = __builtin_amdgcn_fmed3f(c, -448.f, 448.f); d = __builtin_amdgcn_fmed3f(d, -448.f, 448.f);
;     unsigned w = 0u; w = __builtin_amdgcn_cvt_pk_fp8_f32(a, b, w, false); w = __builtin_amdgcn_cvt_pk_fp8_f32(c, d, w, true); return w;
; }
; __device__ __forceinline__ void titem_process(const TItem& t, const f32x4 (&v)[2][8], const f32x4 (&g)[2], int lane) {
;     const int n4 = lane & 7, kr = lane >> 3;
;     float s[8];
; #pragma unroll
;     for (int j = 0; j < 8; ++j) s[j] = t.gain ? g[j >> 2][j & 3] * t.scale : t.scale;
;     if (t.fp8 == 1) {
; #pragma unroll
;         for (int h = 0; h < 2; ++h)
; #pragma unroll
;             for (int i = 0; i < 4; ++i) { u32x2 o; o.x = epi::pk4_fp8(v[h][0][i] * s[0], v[h][1][i] * s[1], v[h][2][i] * s[2], v[h][3][i] * s[3]); o.y = epi::pk4_fp8(v[h][4][i] * s[4], v[h][5][i] * s[5], v[h][6][i] * s[6], v[h][7][i] * s[7]);
;                 __builtin_nontemporal_store(o, (u32x2*)(t.dst + (size_t)(32 * h + 4 * n4 + i) * t.ldwt + 8 * kr)); }
	v_mov_b32_e32 v226, 0x44000000
	v_mov_b32_e32 v227, 0x44000000
	v_mov_b32_e32 v228, 0x44000000
	v_mov_b32_e32 v229, 0x44000000
	v_mov_b32_e32 v230, 0x44000000
	v_mov_b32_e32 v231, 0x44000000
	v_mov_b32_e32 v232, 0x44000000
	v_mov_b32_e32 v233, 0x44000000
	v_pk_mul_f32 v[128:129], v[128:129], v[226:227] op_sel:[0,0] op_sel_hi:[1,0]
	v_pk_mul_f32 v[132:133], v[132:133], v[226:227] op_sel:[0,1] op_sel_hi:[1,1]
	v_pk_mul_f32 v[136:137], v[136:137], v[228:229] op_sel:[0,0] op_sel_hi:[1,0]
	v_pk_mul_f32 v[140:141], v[140:141], v[228:229] op_sel:[0,1] op_sel_hi:[1,1]
	v_pk_mul_f32 v[144:145], v[144:145], v[230:231] op_sel:[0,0] op_sel_hi:[1,0]
	v_pk_mul_f32 v[148:149], v[148:149], v[230:231] op_sel:[0,1] op_sel_hi:[1,1]
	v_pk_mul_f32 v[152:153], v[152:153], v[232:233] op_sel:[0,0] op_sel_hi:[1,0]
	v_pk_mul_f32 v[156:157], v[156:157], v[232:233] op_sel:[0,1] op_sel_hi:[1,1]
	v_pk_mul_f32 v[130:131], v[130:131], v[226:227] op_sel:[0,0] op_sel_hi:[1,0]
	v_pk_mul_f32 v[134:135], v[134:135], v[226:227] op_sel:[0,1] op_sel_hi:[1,1]
	v_pk_mul_f32 v[138:139], v[138:139], v[228:229] op_sel:[0,0] op_sel_hi:[1,0]
	v_pk_mul_f32 v[142:143], v[142:143], v[228:229] op_sel:[0,1] op_sel_hi:[1,1]
	v_pk_mul_f32 v[146:147], v[146:147], v[230:231] op_sel:[0,0] op_sel_hi:[1,0]
	v_pk_mul_f32 v[150:151], v[150:151], v[230:231] op_sel:[0,1] op_sel_hi:[1,1]
	v_pk_mul_f32 v[154:155], v[154:155], v[232:233] op_sel:[0,0] op_sel_hi:[1,0]
	v_pk_mul_f32 v[158:159], v[158:159], v[232:233] op_sel:[0,1] op_sel_hi:[1,1]
	v_pk_mul_f32 v[160:161], v[160:161], v[226:227] op_sel:[0,0] op_sel_hi:[1,0]
	v_pk_mul_f32 v[164:165], v[164:165], v[226:227] op_sel:[0,1] op_sel_hi:[1,1]
	v_pk_mul_f32 v[168:169], v[168:169], v[228:229] op_sel:[0,0] op_sel_hi:[1,0]
	v_pk_mul_f32 v[172:173], v[172:173], v[228:229] op_sel:[0,1] op_sel_hi:[1,1]
	v_pk_mul_f32 v[176:177], v[176:177], v[230:231] op_sel:[0,0] op_sel_hi:[1,0]
	v_pk_mul_f32 v[180:181], v[180:181], v[230:231] op_sel:[0,1] op_sel_hi:[1,1]
	v_pk_mul_f32 v[184:185], v[184:185], v[232:233] op_sel:[0,0] op_sel_hi:[1,0]
	v_pk_mul_f32 v[188:189], v[188:189], v[232:233] op_sel:[0,1] op_sel_hi:[1,1]
	v_pk_mul_f32 v[162:163], v[162:163], v[226:227] op_sel:[0,0] op_sel_hi:[1,0]
	v_pk_mul_f32 v[166:167], v[166:167], v[226:227] op_sel:[0,1] op_sel_hi:[1,1]
	v_pk_mul_f32 v[170:171], v[170:171], v[228:229] op_sel:[0,0] op_sel_hi:[1,0]
	v_pk_mul_f32 v[174:175], v[174:175], v[228:229] op_sel:[0,1] op_sel_hi:[1,1]
	v_pk_mul_f32 v[178:179], v[178:179], v[230:231] op_sel:[0,0] op_sel_hi:[1,0]
	v_pk_mul_f32 v[182:183], v[182:183], v[230:231] op_sel:[0,1] op_sel_hi:[1,1]
	v_pk_mul_f32 v[186:187], v[186:187], v[232:233] op_sel:[0,0] op_sel_hi:[1,0]
	v_pk_mul_f32 v[190:191], v[190:191], v[232:233] op_sel:[0,1] op_sel_hi:[1,1]
	v_med3_f32 v128, v128, s33, v225
	v_med3_f32 v129, v129, s33, v225
	v_med3_f32 v130, v130, s33, v225
	v_med3_f32 v131, v131, s33, v225
	v_med3_f32 v132, v132, s33, v225
	v_med3_f32 v133, v133, s33, v225
	v_med3_f32 v134, v134, s33, v225
	v_med3_f32 v135, v135, s33, v225
	v_med3_f32 v136, v136, s33, v225
	v_med3_f32 v137, v137, s33, v225
	v_med3_f32 v138, v138, s33, v225
	v_med3_f32 v139, v139, s33, v225
	v_med3_f32 v140, v140, s33, v225
	v_med3_f32 v141, v141, s33, v225
	v_med3_f32 v142, v142, s33, v225
	v_med3_f32 v143, v143, s33, v225
	v_med3_f32 v144, v144, s33, v225
	v_med3_f32 v145, v145, s33, v225
	v_med3_f32 v146, v146, s33, v225
	v_med3_f32 v147, v147, s33, v225
	v_med3_f32 v148, v148, s33, v225
	v_med3_f32 v149, v149, s33, v225
	v_med3_f32 v150, v150, s33, v225
	v_med3_f32 v151, v151, s33, v225
	v_med3_f32 v152, v152, s33, v225
	v_med3_f32 v153, v153, s33, v225
	v_med3_f32 v154, v154, s33, v225
	v_med3_f32 v155, v155, s33, v225
	v_med3_f32 v156, v156, s33, v225
	v_med3_f32 v157, v157, s33, v225
	v_med3_f32 v158, v158, s33, v225
	v_med3_f32 v159, v159, s33, v225
	v_med3_f32 v160, v160, s33, v225
	v_med3_f32 v161, v161, s33, v225
	v_med3_f32 v162, v162, s33, v225
	v_med3_f32 v163, v163, s33, v225
	v_med3_f32 v164, v164, s33, v225
	v_med3_f32 v165, v165, s33, v225
	v_med3_f32 v166, v166, s33, v225
	v_med3_f32 v167, v167, s33, v225
	v_med3_f32 v168, v168, s33, v225
	v_med3_f32 v169, v169, s33, v225
	v_med3_f32 v170, v170, s33, v225
	v_med3_f32 v171, v171, s33, v225
	v_med3_f32 v172, v172, s33, v225
	v_med3_f32 v173, v173, s33, v225
	v_med3_f32 v174, v174, s33, v225
	v_med3_f32 v175, v175, s33, v225
	v_med3_f32 v176, v176, s33, v225
	v_med3_f32 v177, v177, s33, v225
	v_med3_f32 v178, v178, s33, v225
	v_med3_f32 v179, v179, s33, v225
	v_med3_f32 v180, v180, s33, v225
	v_med3_f32 v181, v181, s33, v225
	v_med3_f32 v182, v182, s33, v225
	v_med3_f32 v183, v183, s33, v225
	v_med3_f32 v184, v184, s33, v225
	v_med3_f32 v185, v185, s33, v225
	v_med3_f32 v186, v186, s33, v225
	v_med3_f32 v187, v187, s33, v225
	v_med3_f32 v188, v188, s33, v225
	v_med3_f32 v189, v189, s33, v225
	v_med3_f32 v190, v190, s33, v225
	v_med3_f32 v191, v191, s33, v225
	v_cvt_pk_fp8_f32 v234, v128, v132
	v_cvt_pk_fp8_f32 v235, v144, v148
	v_cvt_pk_fp8_f32 v234, v136, v140 op_sel:[0,0,1]
	v_cvt_pk_fp8_f32 v235, v152, v156 op_sel:[0,0,1]
	s_nop 0
	global_store_dwordx2 v224, v[234:235], s[42:43] nt
	v_cvt_pk_fp8_f32 v236, v129, v133
	v_cvt_pk_fp8_f32 v237, v145, v149
	v_cvt_pk_fp8_f32 v236, v137, v141 op_sel:[0,0,1]
	v_cvt_pk_fp8_f32 v237, v153, v157 op_sel:[0,0,1]
	v_add_u32_e32 v238, 0x1c00, v224
	global_store_dwordx2 v238, v[236:237], s[42:43] nt
	v_cvt_pk_fp8_f32 v234, v130, v134
	v_cvt_pk_fp8_f32 v235, v146, v150
	v_cvt_pk_fp8_f32 v234, v138, v142 op_sel:[0,0,1]
	v_cvt_pk_fp8_f32 v235, v154, v158 op_sel:[0,0,1]
	v_add_u32_e32 v238, 0x3800, v224
; __device__ __forceinline__ bool titem_group(int& it, TItem& t, const float* W, size_t wstride, int nmat, int K, int N, const float* gain, float scale, void* WT, size_t tstride_bytes, int mode, int fp8) {
;     const int nblk = N / 64, per = (K / 64) * nblk, tot = per * nmat;
;     if (it >= tot) { it -= tot; return false; }
;     const int mat = it / per, r = it % per, k0 = 64 * (r / nblk), n0 = 64 * (r % nblk), esz = (fp8 == 1) ? 1 : 2;
;     const int drow0 = (mode == 0) ? n0 : (256 * (n0 / 128) + (n0 % 128) + (mode == 2 ? 128 : 0));
;     t.src = W + (size_t)mat * wstride + (size_t)k0 * N + n0; t.gain = gain ? gain + k0 : nullptr;
;     t.dst = (unsigned char*)WT + (size_t)mat * tstride_bytes + ((size_t)drow0 * K + k0) * esz; t.ldw = N; t.ldwt = K * esz; t.fp8 = fp8; t.scale = scale; return true;
; }
; __device__ __forceinline__ void titem_load(const TItem& t, f32x4 (&v)[2][8], f32x4 (&g)[2], int lane) {
;     const int n4 = lane & 7, kr = lane >> 3;
;     const float* gp = t.gain ? t.gain : t.src;
; #pragma unroll
;     for (int h = 0; h < 2; ++h)
; #pragma unroll
;         for (int i = 0; i < 8; ++i) v[h][i] = *(const f32x4*)(t.src + (size_t)(8 * kr + i) * t.ldw + 32 * h + 4 * n4);
;     g[0] = *(const f32x4*)(gp + 8 * kr); g[1] = *(const f32x4*)(gp + 8 * kr + 4);
; }
; __device__ __forceinline__ void titem_process(const TItem& t, const f32x4 (&v)[2][8], const f32x4 (&g)[2], int lane) {
;     const int n4 = lane & 7, kr = lane >> 3;
;     float s[8];
; #pragma unroll
;     for (int j = 0; j < 8; ++j) s[j] = t.gain ? g[j >> 2][j & 3] * t.scale : t.scale;
;     if (t.fp8 == 1) {
; #pragma unroll
;         for (int h = 0; h < 2; ++h)
; #pragma unroll
;             for (int i = 0; i < 4; ++i) { u32x2 o; o.x = epi::pk4_fp8(v[h][0][i] * s[0], v[h][1][i] * s[1], v[h][2][i] * s[2], v[h][3][i] * s[3]); o.y = epi::pk4_fp8(v[h][4][i] * s[4], v[h][5][i] * s[5], v[h][6][i] * s[6], v[h][7][i] * s[7]);
;                 __builtin_nontemporal_store(o, (u32x2*)(t.dst + (size_t)(32 * h + 4 * n4 + i) * t.ldwt + 8 * kr)); }
	global_store_dwordx2 v238, v[234:235], s[42:43] nt
	v_cvt_pk_fp8_f32 v236, v131, v135
	v_cvt_pk_fp8_f32 v237, v147, v151
	v_cvt_pk_fp8_f32 v236, v139, v143 op_sel:[0,0,1]
	v_cvt_pk_fp8_f32 v237, v155, v159 op_sel:[0,0,1]
	v_add_u32_e32 v238, 0x5400, v224
	global_store_dwordx2 v238, v[236:237], s[42:43] nt
	v_cvt_pk_fp8_f32 v234, v160, v164
	v_cvt_pk_fp8_f32 v235, v176, v180
	v_cvt_pk_fp8_f32 v234, v168, v172 op_sel:[0,0,1]
	v_cvt_pk_fp8_f32 v235, v184, v188 op_sel:[0,0,1]
	v_add_u32_e32 v238, 0x38000, v224
	global_store_dwordx2 v238, v[234:235], s[42:43] nt
	v_cvt_pk_fp8_f32 v236, v161, v165
	v_cvt_pk_fp8_f32 v237, v177, v181
	v_cvt_pk_fp8_f32 v236, v169, v173 op_sel:[0,0,1]
	v_cvt_pk_fp8_f32 v237, v185, v189 op_sel:[0,0,1]
	v_add_u32_e32 v238, 0x39c00, v224
	global_store_dwordx2 v238, v[236:237], s[42:43] nt
	v_cvt_pk_fp8_f32 v234, v162, v166
	v_cvt_pk_fp8_f32 v235, v178, v182
	v_cvt_pk_fp8_f32 v234, v170, v174 op_sel:[0,0,1]
	v_cvt_pk_fp8_f32 v235, v186, v190 op_sel:[0,0,1]
	v_add_u32_e32 v238, 0x3b800, v224
	global_store_dwordx2 v238, v[234:235], s[42:43] nt
	v_cvt_pk_fp8_f32 v236, v163, v167
	v_cvt_pk_fp8_f32 v237, v179, v183
	v_cvt_pk_fp8_f32 v236, v171, v175 op_sel:[0,0,1]
	v_cvt_pk_fp8_f32 v237, v187, v191 op_sel:[0,0,1]
	v_add_u32_e32 v238, 0x3d400, v224
	global_store_dwordx2 v238, v[236:237], s[42:43] nt
	s_add_i32 s35, s27, 4
	s_min_u32 s35, s35, 13
	s_lshl_b32 s37, s35, 11
	s_add_i32 s37, s37, s25
	s_lshr_b32 s45, s37, 9
	s_mul_i32 s45, s45, 0x2493
	s_lshr_b32 s45, s45, 16
	s_mul_i32 s51, s45, 0xe00
	s_sub_i32 s50, s37, s51
	s_lshr_b32 s51, s50, 5
	s_and_b32 s52, s50, 31
	s_mul_i32 s63, s45, 0x3800000
	s_add_u32 s46, s4, s63
	s_addc_u32 s47, s5, 0
	s_lshl_b32 s63, s51, 19
	s_lshl_b32 s37, s52, 8
	s_add_i32 s63, s63, s37
	s_add_u32 s46, s46, s63
	s_addc_u32 s47, s47, 0
	s_mov_b64 s[48:49], s[4:5]
	s_mul_i32 s63, s45, 0xe00000
	s_mul_i32 s37, s52, 0x70000
	s_add_i32 s63, s63, s37
	s_lshl_b32 s37, s51, 6
	s_add_i32 s63, s63, s37
	s_add_u32 s42, s8, s63
	s_addc_u32 s43, s9, 0
	global_load_dwordx4 v[128:131], v221, s[46:47]
	global_load_dwordx4 v[160:163], v221, s[46:47] offset:128
	v_add_u32_e32 v238, 0x2000, v221
	global_load_dwordx4 v[132:135], v238, s[46:47]
	global_load_dwordx4 v[164:167], v238, s[46:47] offset:128
	v_add_u32_e32 v238, 0x4000, v221
	global_load_dwordx4 v[136:139], v238, s[46:47]
	global_load_dwordx4 v[168:171], v238, s[46:47] offset:128
	v_add_u32_e32 v238, 0x6000, v221
	global_load_dwordx4 v[140:143], v238, s[46:47]
	global_load_dwordx4 v[172:175], v238, s[46:47] offset:128
	v_add_u32_e32 v238, 0x8000, v221
	global_load_dwordx4 v[144:147], v238, s[46:47]
	global_load_dwordx4 v[176:179], v238, s[46:47] offset:128
	v_add_u32_e32 v238, 0xa000, v221
	global_load_dwordx4 v[148:151], v238, s[46:47]
	global_load_dwordx4 v[180:183], v238, s[46:47] offset:128
	v_add_u32_e32 v238, 0xc000, v221
	global_load_dwordx4 v[152:155], v238, s[46:47]
	global_load_dwordx4 v[184:187], v238, s[46:47] offset:128
	v_add_u32_e32 v238, 0xe000, v221
	global_load_dwordx4 v[156:159], v238, s[46:47]
	global_load_dwordx4 v[188:191], v238, s[46:47] offset:128
	global_load_dwordx4 v[212:215], v222, s[48:49]
	global_load_dwordx4 v[216:219], v222, s[48:49] offset:16
	s_waitcnt vmcnt(44)
; __device__ __forceinline__ void titem_process(const TItem& t, const f32x4 (&v)[2][8], const f32x4 (&g)[2], int lane) {
;     const int n4 = lane & 7, kr = lane >> 3;
;     float s[8];
; #pragma unroll
;     for (int j = 0; j < 8; ++j) s[j] = t.gain ? g[j >> 2][j & 3] * t.scale : t.scale;
;     if (t.fp8 == 1) {
; #pragma unroll
;         for (int h = 0; h < 2; ++h)
; #pragma unroll
;             for (int i = 0; i < 4; ++i) { u32x2 o; o.x = epi::pk4_fp8(v[h][0][i] * s[0], v[h][1][i] * s[1], v[h][2][i] * s[2], v[h][3][i] * s[3]); o.y = epi::pk4_fp8(v[h][4][i] * s[4], v[h][5][i] * s[5], v[h][6][i] * s[6], v[h][7][i] * s[7]);
;                 __builtin_nontemporal_store(o, (u32x2*)(t.dst + (size_t)(32 * h + 4 * n4 + i) * t.ldwt + 8 * kr)); }
	v_mov_b32_e32 v226, 0x44000000
	v_mov_b32_e32 v227, 0x44000000
	v_mov_b32_e32 v228, 0x44000000
	v_mov_b32_e32 v229, 0x44000000
	v_mov_b32_e32 v230, 0x44000000
	v_mov_b32_e32 v231, 0x44000000
	v_mov_b32_e32 v232, 0x44000000
	v_mov_b32_e32 v233, 0x44000000
	v_pk_mul_f32 v[0:1], v[0:1], v[226:227] op_sel:[0,0] op_sel_hi:[1,0]
	v_pk_mul_f32 v[4:5], v[4:5], v[226:227] op_sel:[0,1] op_sel_hi:[1,1]
	v_pk_mul_f32 v[8:9], v[8:9], v[228:229] op_sel:[0,0] op_sel_hi:[1,0]
	v_pk_mul_f32 v[12:13], v[12:13], v[228:229] op_sel:[0,1] op_sel_hi:[1,1]
	v_pk_mul_f32 v[16:17], v[16:17], v[230:231] op_sel:[0,0] op_sel_hi:[1,0]
	v_pk_mul_f32 v[20:21], v[20:21], v[230:231] op_sel:[0,1] op_sel_hi:[1,1]
	v_pk_mul_f32 v[24:25], v[24:25], v[232:233] op_sel:[0,0] op_sel_hi:[1,0]
	v_pk_mul_f32 v[28:29], v[28:29], v[232:233] op_sel:[0,1] op_sel_hi:[1,1]
	v_pk_mul_f32 v[2:3], v[2:3], v[226:227] op_sel:[0,0] op_sel_hi:[1,0]
	v_pk_mul_f32 v[6:7], v[6:7], v[226:227] op_sel:[0,1] op_sel_hi:[1,1]
	v_pk_mul_f32 v[10:11], v[10:11], v[228:229] op_sel:[0,0] op_sel_hi:[1,0]
	v_pk_mul_f32 v[14:15], v[14:15], v[228:229] op_sel:[0,1] op_sel_hi:[1,1]
	v_pk_mul_f32 v[18:19], v[18:19], v[230:231] op_sel:[0,0] op_sel_hi:[1,0]
	v_pk_mul_f32 v[22:23], v[22:23], v[230:231] op_sel:[0,1] op_sel_hi:[1,1]
	v_pk_mul_f32 v[26:27], v[26:27], v[232:233] op_sel:[0,0] op_sel_hi:[1,0]
	v_pk_mul_f32 v[30:31], v[30:31], v[232:233] op_sel:[0,1] op_sel_hi:[1,1]
	v_pk_mul_f32 v[32:33], v[32:33], v[226:227] op_sel:[0,0] op_sel_hi:[1,0]
	v_pk_mul_f32 v[36:37], v[36:37], v[226:227] op_sel:[0,1] op_sel_hi:[1,1]
	v_pk_mul_f32 v[40:41], v[40:41], v[228:229] op_sel:[0,0] op_sel_hi:[1,0]
	v_pk_mul_f32 v[44:45], v[44:45], v[228:229] op_sel:[0,1] op_sel_hi:[1,1]
	v_pk_mul_f32 v[48:49], v[48:49], v[230:231] op_sel:[0,0] op_sel_hi:[1,0]
	v_pk_mul_f32 v[52:53], v[52:53], v[230:231] op_sel:[0,1] op_sel_hi:[1,1]
	v_pk_mul_f32 v[56:57], v[56:57], v[232:233] op_sel:[0,0] op_sel_hi:[1,0]
	v_pk_mul_f32 v[60:61], v[60:61], v[232:233] op_sel:[0,1] op_sel_hi:[1,1]
	v_pk_mul_f32 v[34:35], v[34:35], v[226:227] op_sel:[0,0] op_sel_hi:[1,0]
	v_pk_mul_f32 v[38:39], v[38:39], v[226:227] op_sel:[0,1] op_sel_hi:[1,1]
	v_pk_mul_f32 v[42:43], v[42:43], v[228:229] op_sel:[0,0] op_sel_hi:[1,0]
	v_pk_mul_f32 v[46:47], v[46:47], v[228:229] op_sel:[0,1] op_sel_hi:[1,1]
	v_pk_mul_f32 v[50:51], v[50:51], v[230:231] op_sel:[0,0] op_sel_hi:[1,0]
	v_pk_mul_f32 v[54:55], v[54:55], v[230:231] op_sel:[0,1] op_sel_hi:[1,1]
	v_pk_mul_f32 v[58:59], v[58:59], v[232:233] op_sel:[0,0] op_sel_hi:[1,0]
	v_pk_mul_f32 v[62:63], v[62:63], v[232:233] op_sel:[0,1] op_sel_hi:[1,1]
	v_med3_f32 v0, v0, s33, v225
	v_med3_f32 v1, v1, s33, v225
	v_med3_f32 v2, v2, s33, v225
	v_med3_f32 v3, v3, s33, v225
	v_med3_f32 v4, v4, s33, v225
	v_med3_f32 v5, v5, s33, v225
	v_med3_f32 v6, v6, s33, v225
	v_med3_f32 v7, v7, s33, v225
	v_med3_f32 v8, v8, s33, v225
	v_med3_f32 v9, v9, s33, v225
	v_med3_f32 v10, v10, s33, v225
	v_med3_f32 v11, v11, s33, v225
	v_med3_f32 v12, v12, s33, v225
	v_med3_f32 v13, v13, s33, v225
	v_med3_f32 v14, v14, s33, v225
	v_med3_f32 v15, v15, s33, v225
	v_med3_f32 v16, v16, s33, v225
	v_med3_f32 v17, v17, s33, v225
	v_med3_f32 v18, v18, s33, v225
	v_med3_f32 v19, v19, s33, v225
	v_med3_f32 v20, v20, s33, v225
	v_med3_f32 v21, v21, s33, v225
	v_med3_f32 v22, v22, s33, v225
	v_med3_f32 v23, v23, s33, v225
	v_med3_f32 v24, v24, s33, v225
	v_med3_f32 v25, v25, s33, v225
	v_med3_f32 v26, v26, s33, v225
	v_med3_f32 v27, v27, s33, v225
	v_med3_f32 v28, v28, s33, v225
	v_med3_f32 v29, v29, s33, v225
	v_med3_f32 v30, v30, s33, v225
	v_med3_f32 v31, v31, s33, v225
	v_med3_f32 v32, v32, s33, v225
	v_med3_f32 v33, v33, s33, v225
	v_med3_f32 v34, v34, s33, v225
	v_med3_f32 v35, v35, s33, v225
	v_med3_f32 v36, v36, s33, v225
	v_med3_f32 v37, v37, s33, v225
	v_med3_f32 v38, v38, s33, v225
	v_med3_f32 v39, v39, s33, v225
	v_med3_f32 v40, v40, s33, v225
	v_med3_f32 v41, v41, s33, v225
	v_med3_f32 v42, v42, s33, v225
	v_med3_f32 v43, v43, s33, v225
	v_med3_f32 v44, v44, s33, v225
	v_med3_f32 v45, v45, s33, v225
	v_med3_f32 v46, v46, s33, v225
	v_med3_f32 v47, v47, s33, v225
	v_med3_f32 v48, v48, s33, v225
	v_med3_f32 v49, v49, s33, v225
	v_med3_f32 v50, v50, s33, v225
	v_med3_f32 v51, v51, s33, v225
	v_med3_f32 v52, v52, s33, v225
	v_med3_f32 v53, v53, s33, v225
	v_med3_f32 v54, v54, s33, v225
	v_med3_f32 v55, v55, s33, v225
	v_med3_f32 v56, v56, s33, v225
	v_med3_f32 v57, v57, s33, v225
	v_med3_f32 v58, v58, s33, v225
	v_med3_f32 v59, v59, s33, v225
	v_med3_f32 v60, v60, s33, v225
	v_med3_f32 v61, v61, s33, v225
	v_med3_f32 v62, v62, s33, v225
	v_med3_f32 v63, v63, s33, v225
	v_cvt_pk_fp8_f32 v234, v0, v4
	v_cvt_pk_fp8_f32 v235, v16, v20
	v_cvt_pk_fp8_f32 v234, v8, v12 op_sel:[0,0,1]
	v_cvt_pk_fp8_f32 v235, v24, v28 op_sel:[0,0,1]
	s_nop 0
	global_store_dwordx2 v224, v[234:235], s[38:39] nt
	v_cvt_pk_fp8_f32 v236, v1, v5
	v_cvt_pk_fp8_f32 v237, v17, v21
	v_cvt_pk_fp8_f32 v236, v9, v13 op_sel:[0,0,1]
	v_cvt_pk_fp8_f32 v237, v25, v29 op_sel:[0,0,1]
	v_add_u32_e32 v238, 0x1c00, v224
	global_store_dwordx2 v238, v[236:237], s[38:39] nt
	v_cvt_pk_fp8_f32 v234, v2, v6
	v_cvt_pk_fp8_f32 v235, v18, v22
	v_cvt_pk_fp8_f32 v234, v10, v14 op_sel:[0,0,1]
	v_cvt_pk_fp8_f32 v235, v26, v30 op_sel:[0,0,1]
	v_add_u32_e32 v238, 0x3800, v224
	global_store_dwordx2 v238, v[234:235], s[38:39] nt
	v_cvt_pk_fp8_f32 v236, v3, v7
	v_cvt_pk_fp8_f32 v237, v19, v23
	v_cvt_pk_fp8_f32 v236, v11, v15 op_sel:[0,0,1]
	v_cvt_pk_fp8_f32 v237, v27, v31 op_sel:[0,0,1]
	v_add_u32_e32 v238, 0x5400, v224
	global_store_dwordx2 v238, v[236:237], s[38:39] nt
	v_cvt_pk_fp8_f32 v234, v32, v36
	v_cvt_pk_fp8_f32 v235, v48, v52
	v_cvt_pk_fp8_f32 v234, v40, v44 op_sel:[0,0,1]
	v_cvt_pk_fp8_f32 v235, v56, v60 op_sel:[0,0,1]
	v_add_u32_e32 v238, 0x38000, v224
	global_store_dwordx2 v238, v[234:235], s[38:39] nt
	v_cvt_pk_fp8_f32 v236, v33, v37
	v_cvt_pk_fp8_f32 v237, v49, v53
	v_cvt_pk_fp8_f32 v236, v41, v45 op_sel:[0,0,1]
	v_cvt_pk_fp8_f32 v237, v57, v61 op_sel:[0,0,1]
	v_add_u32_e32 v238, 0x39c00, v224
	global_store_dwordx2 v238, v[236:237], s[38:39] nt
	v_cvt_pk_fp8_f32 v234, v34, v38
	v_cvt_pk_fp8_f32 v235, v50, v54
	v_cvt_pk_fp8_f32 v234, v42, v46 op_sel:[0,0,1]
	v_cvt_pk_fp8_f32 v235, v58, v62 op_sel:[0,0,1]
	v_add_u32_e32 v238, 0x3b800, v224
	global_store_dwordx2 v238, v[234:235], s[38:39] nt
	v_cvt_pk_fp8_f32 v236, v35, v39
	v_cvt_pk_fp8_f32 v237, v51, v55
	v_cvt_pk_fp8_f32 v236, v43, v47 op_sel:[0,0,1]
	v_cvt_pk_fp8_f32 v237, v59, v63 op_sel:[0,0,1]
	v_add_u32_e32 v238, 0x3d400, v224
	global_store_dwordx2 v238, v[236:237], s[38:39] nt
	s_add_i32 s27, s27, 3
	s_sub_i32 s30, s30, 1
	s_cmp_lg_u32 s30, 0
	s_cbranch_scc1 .Lcv1_dn
	s_waitcnt vmcnt(0)

; __device__ __forceinline__ bool titem_group(int& it, TItem& t, const float* W, size_t wstride, int nmat, int K, int N, const float* gain, float scale, void* WT, size_t tstride_bytes, int mode, int fp8) {
;     const int nblk = N / 64, per = (K / 64) * nblk, tot = per * nmat;
;     if (it >= tot) { it -= tot; return false; }
;     const int mat = it / per, r = it % per, k0 = 64 * (r / nblk), n0 = 64 * (r % nblk), esz = (fp8 == 1) ? 1 : 2;
;     const int drow0 = (mode == 0) ? n0 : (256 * (n0 / 128) + (n0 % 128) + (mode == 2 ? 128 : 0));
;     t.src = W + (size_t)mat * wstride + (size_t)k0 * N + n0; t.gain = gain ? gain + k0 : nullptr;
;     t.dst = (unsigned char*)WT + (size_t)mat * tstride_bytes + ((size_t)drow0 * K + k0) * esz; t.ldw = N; t.ldwt = K * esz; t.fp8 = fp8; t.scale = scale; return true;
; }
; __device__ __forceinline__ void titem_load(const TItem& t, f32x4 (&v)[2][8], f32x4 (&g)[2], int lane) {
;     const int n4 = lane & 7, kr = lane >> 3;
;     const float* gp = t.gain ? t.gain : t.src;
; #pragma unroll
;     for (int h = 0; h < 2; ++h)
; #pragma unroll
;         for (int i = 0; i < 8; ++i) v[h][i] = *(const f32x4*)(t.src + (size_t)(8 * kr + i) * t.ldw + 32 * h + 4 * n4);
;     g[0] = *(const f32x4*)(gp + 8 * kr); g[1] = *(const f32x4*)(gp + 8 * kr + 4);
; }
; __global__ void __launch_bounds__(NTHR, 2) fwd_kernel(Args args) {
;     ...
;         if (half == 0) { __syncthreads(); CONVERT_RANGE(0, NEXP_ITEMS); }
.LBB0_942:
	v_readlane_b32 s0, v254, 52
	v_readlane_b32 s1, v254, 53
	s_and_b64 vcc, exec, s[0:1]
	s_cbranch_vccz .LBB0_1082
	v_readlane_b32 s0, v254, 54
	v_readlane_b32 s1, v254, 55
	s_and_b64 vcc, exec, s[0:1]
	s_waitcnt vmcnt(0) lgkmcnt(0)
	s_barrier
	s_cbranch_vccnz .LBB0_1082
	s_load_dwordx2 s[2:3], s[66:67], 0xb0
	s_load_dwordx2 s[4:5], s[66:67], 0xc0
	s_load_dwordx2 s[6:7], s[66:67], 0xc8
	s_load_dwordx2 s[8:9], s[66:67], 0xe0
	v_readlane_b32 s25, v254, 12
	v_mbcnt_lo_u32_b32 v239, -1, 0
	v_mbcnt_hi_u32_b32 v239, -1, v239
	v_and_b32_e32 v237, 7, v239
	v_lshrrev_b32_e32 v203, 3, v239
	v_mul_u32_u24_e32 v220, 0x38000, v203
	v_lshl_add_u32 v220, v237, 4, v220
	v_lshlrev_b32_e32 v221, 16, v203
	v_lshl_add_u32 v221, v237, 4, v221
	v_lshlrev_b32_e32 v222, 5, v203
	v_lshlrev_b32_e32 v223, 13, v237
	v_lshl_add_u32 v223, v203, 3, v223
	v_mul_u32_u24_e32 v224, 0x7000, v237
	v_lshl_add_u32 v224, v203, 3, v224
	v_mov_b32_e32 v225, 0x43e00000
	s_mov_b32 s33, 0xc3e00000
	s_waitcnt lgkmcnt(0)
	s_add_u32 s8, s8, 0xb000000
	s_addc_u32 s9, s9, 0
	s_mov_b32 s35, 0
	s_lshl_b32 s37, s35, 11
	s_add_i32 s37, s37, s25
	s_lshr_b32 s45, s37, 9
	s_mul_i32 s45, s45, 0x2493
	s_lshr_b32 s45, s45, 16
	s_mul_i32 s51, s45, 0xe00
	s_sub_i32 s50, s37, s51
	s_lshr_b32 s51, s50, 4
	s_mul_i32 s51, s51, 0x2493
	s_lshr_b32 s51, s51, 16
	s_mul_i32 s53, s51, 0x70
	s_sub_i32 s52, s50, s53
	s_and_b32 s53, s45, 7
	s_lshr_b32 s60, s45, 3
	s_cmp_lg_u32 s60, 0
	s_cselect_b32 s46, s6, s4
	s_cselect_b32 s47, s7, s5
	s_mul_i32 s63, s53, 0x3800000
	s_add_u32 s46, s46, s63
	s_addc_u32 s47, s47, 0
	s_mul_i32 s63, s51, 0x1c0000
	s_lshl_b32 s37, s52, 8
	s_add_i32 s63, s63, s37
	s_add_u32 s46, s46, s63
	s_addc_u32 s47, s47, 0
	s_lshl_b32 s63, s51, 8
	s_add_u32 s48, s2, s63
	s_addc_u32 s49, s3, 0
	s_mul_i32 s63, s53, 0x1c00000
	s_lshr_b32 s37, s52, 1
	s_lshl_b32 s37, s37, 19
	s_add_i32 s63, s63, s37
	s_and_b32 s37, s52, 1
	s_lshl_b32 s37, s37, 17
	s_add_i32 s63, s63, s37
	s_lshl_b32 s37, s60, 18
	s_add_i32 s63, s63, s37
	s_lshl_b32 s37, s51, 6
	s_add_i32 s63, s63, s37
	s_add_u32 s38, s8, s63
	s_addc_u32 s39, s9, 0
	global_load_dwordx4 v[0:3], v220, s[46:47]
	global_load_dwordx4 v[32:35], v220, s[46:47] offset:128
	v_add_u32_e32 v238, 0x7000, v220
	global_load_dwordx4 v[4:7], v238, s[46:47]
	global_load_dwordx4 v[36:39], v238, s[46:47] offset:128
	v_add_u32_e32 v238, 0xe000, v220
	global_load_dwordx4 v[8:11], v238, s[46:47]
	global_load_dwordx4 v[40:43], v238, s[46:47] offset:128
	v_add_u32_e32 v238, 0x15000, v220
	global_load_dwordx4 v[12:15], v238, s[46:47]
	global_load_dwordx4 v[44:47], v238, s[46:47] offset:128
	v_add_u32_e32 v238, 0x1c000, v220
	global_load_dwordx4 v[16:19], v238, s[46:47]
	global_load_dwordx4 v[48:51], v238, s[46:47] offset:128
	v_add_u32_e32 v238, 0x23000, v220
	global_load_dwordx4 v[20:23], v238, s[46:47]
	global_load_dwordx4 v[52:55], v238, s[46:47] offset:128
	v_add_u32_e32 v238, 0x2a000, v220
	global_load_dwordx4 v[24:27], v238, s[46:47]
	global_load_dwordx4 v[56:59], v238, s[46:47] offset:128
	v_add_u32_e32 v238, 0x31000, v220
	global_load_dwordx4 v[28:31], v238, s[46:47]
	global_load_dwordx4 v[60:63], v238, s[46:47] offset:128
	global_load_dwordx4 v[192:195], v222, s[48:49]
	global_load_dwordx4 v[196:199], v222, s[48:49] offset:16
	s_mov_b32 s35, 1
	s_lshl_b32 s37, s35, 11
	s_add_i32 s37, s37, s25
	s_lshr_b32 s45, s37, 9
	s_mul_i32 s45, s45, 0x2493
	s_lshr_b32 s45, s45, 16
	s_mul_i32 s51, s45, 0xe00
	s_sub_i32 s50, s37, s51
	s_lshr_b32 s51, s50, 4
	s_mul_i32 s51, s51, 0x2493
	s_lshr_b32 s51, s51, 16
	s_mul_i32 s53, s51, 0x70
	s_sub_i32 s52, s50, s53
	s_and_b32 s53, s45, 7
	s_lshr_b32 s60, s45, 3
	s_cmp_lg_u32 s60, 0
	s_cselect_b32 s46, s6, s4
	s_cselect_b32 s47, s7, s5
	s_mul_i32 s63, s53, 0x3800000
	s_add_u32 s46, s46, s63
	s_addc_u32 s47, s47, 0
	s_mul_i32 s63, s51, 0x1c0000
	s_lshl_b32 s37, s52, 8
	s_add_i32 s63, s63, s37
	s_add_u32 s46, s46, s63
	s_addc_u32 s47, s47, 0
	s_lshl_b32 s63, s51, 8
	s_add_u32 s48, s2, s63
	s_addc_u32 s49, s3, 0
	s_mul_i32 s63, s53, 0x1c00000
	s_lshr_b32 s37, s52, 1
	s_lshl_b32 s37, s37, 19
	s_add_i32 s63, s63, s37
	s_and_b32 s37, s52, 1
	s_lshl_b32 s37, s37, 17
	s_add_i32 s63, s63, s37
	s_lshl_b32 s37, s60, 18
	s_add_i32 s63, s63, s37
	s_lshl_b32 s37, s51, 6
	s_add_i32 s63, s63, s37
	s_add_u32 s40, s8, s63
	s_addc_u32 s41, s9, 0
	global_load_dwordx4 v[64:67], v220, s[46:47]
	global_load_dwordx4 v[96:99], v220, s[46:47] offset:128
	v_add_u32_e32 v238, 0x7000, v220
	global_load_dwordx4 v[68:71], v238, s[46:47]
	global_load_dwordx4 v[100:103], v238, s[46:47] offset:128
	v_add_u32_e32 v238, 0xe000, v220
	global_load_dwordx4 v[72:75], v238, s[46:47]
	global_load_dwordx4 v[104:107], v238, s[46:47] offset:128
	v_add_u32_e32 v238, 0x15000, v220
	global_load_dwordx4 v[76:79], v238, s[46:47]
	global_load_dwordx4 v[108:111], v238, s[46:47] offset:128
	v_add_u32_e32 v238, 0x1c000, v220
	global_load_dwordx4 v[80:83], v238, s[46:47]
	global_load_dwordx4 v[112:115], v238, s[46:47] offset:128
	v_add_u32_e32 v238, 0x23000, v220
	global_load_dwordx4 v[84:87], v238, s[46:47]
	global_load_dwordx4 v[116:119], v238, s[46:47] offset:128
	v_add_u32_e32 v238, 0x2a000, v220
	global_load_dwordx4 v[88:91], v238, s[46:47]
	global_load_dwordx4 v[120:123], v238, s[46:47] offset:128
	v_add_u32_e32 v238, 0x31000, v220
	global_load_dwordx4 v[92:95], v238, s[46:47]
	global_load_dwordx4 v[124:127], v238, s[46:47] offset:128
	global_load_dwordx4 v[204:207], v222, s[48:49]
	global_load_dwordx4 v[208:211], v222, s[48:49] offset:16
	s_mov_b32 s35, 2
	s_lshl_b32 s37, s35, 11
	s_add_i32 s37, s37, s25
	s_lshr_b32 s45, s37, 9
	s_mul_i32 s45, s45, 0x2493
	s_lshr_b32 s45, s45, 16
; __device__ __forceinline__ bool titem_group(int& it, TItem& t, const float* W, size_t wstride, int nmat, int K, int N, const float* gain, float scale, void* WT, size_t tstride_bytes, int mode, int fp8) {
;     const int nblk = N / 64, per = (K / 64) * nblk, tot = per * nmat;
;     if (it >= tot) { it -= tot; return false; }
;     const int mat = it / per, r = it % per, k0 = 64 * (r / nblk), n0 = 64 * (r % nblk), esz = (fp8 == 1) ? 1 : 2;
;     const int drow0 = (mode == 0) ? n0 : (256 * (n0 / 128) + (n0 % 128) + (mode == 2 ? 128 : 0));
;     t.src = W + (size_t)mat * wstride + (size_t)k0 * N + n0; t.gain = gain ? gain + k0 : nullptr;
;     t.dst = (unsigned char*)WT + (size_t)mat * tstride_bytes + ((size_t)drow0 * K + k0) * esz; t.ldw = N; t.ldwt = K * esz; t.fp8 = fp8; t.scale = scale; return true;
; }
; __device__ __forceinline__ void titem_load(const TItem& t, f32x4 (&v)[2][8], f32x4 (&g)[2], int lane) {
;     const int n4 = lane & 7, kr = lane >> 3;
;     const float* gp = t.gain ? t.gain : t.src;
; #pragma unroll
;     for (int h = 0; h < 2; ++h)
; #pragma unroll
;         for (int i = 0; i < 8; ++i) v[h][i] = *(const f32x4*)(t.src + (size_t)(8 * kr + i) * t.ldw + 32 * h + 4 * n4);
;     g[0] = *(const f32x4*)(gp + 8 * kr); g[1] = *(const f32x4*)(gp + 8 * kr + 4);
; }
	s_mul_i32 s51, s45, 0xe00
	s_sub_i32 s50, s37, s51
	s_lshr_b32 s51, s50, 4
	s_mul_i32 s51, s51, 0x2493
	s_lshr_b32 s51, s51, 16
	s_mul_i32 s53, s51, 0x70
	s_sub_i32 s52, s50, s53
	s_and_b32 s53, s45, 7
	s_lshr_b32 s60, s45, 3
	s_cmp_lg_u32 s60, 0
	s_cselect_b32 s46, s6, s4
	s_cselect_b32 s47, s7, s5
	s_mul_i32 s63, s53, 0x3800000
	s_add_u32 s46, s46, s63
	s_addc_u32 s47, s47, 0
	s_mul_i32 s63, s51, 0x1c0000
	s_lshl_b32 s37, s52, 8
	s_add_i32 s63, s63, s37
	s_add_u32 s46, s46, s63
	s_addc_u32 s47, s47, 0
	s_lshl_b32 s63, s51, 8
	s_add_u32 s48, s2, s63
	s_addc_u32 s49, s3, 0
	s_mul_i32 s63, s53, 0x1c00000
	s_lshr_b32 s37, s52, 1
	s_lshl_b32 s37, s37, 19
	s_add_i32 s63, s63, s37
	s_and_b32 s37, s52, 1
	s_lshl_b32 s37, s37, 17
	s_add_i32 s63, s63, s37
	s_lshl_b32 s37, s60, 18
	s_add_i32 s63, s63, s37
	s_lshl_b32 s37, s51, 6
	s_add_i32 s63, s63, s37
	s_add_u32 s42, s8, s63
	s_addc_u32 s43, s9, 0
	global_load_dwordx4 v[128:131], v220, s[46:47]
	global_load_dwordx4 v[160:163], v220, s[46:47] offset:128
	v_add_u32_e32 v238, 0x7000, v220
	global_load_dwordx4 v[132:135], v238, s[46:47]
	global_load_dwordx4 v[164:167], v238, s[46:47] offset:128
	v_add_u32_e32 v238, 0xe000, v220
	global_load_dwordx4 v[136:139], v238, s[46:47]
	global_load_dwordx4 v[168:171], v238, s[46:47] offset:128
	v_add_u32_e32 v238, 0x15000, v220
	global_load_dwordx4 v[140:143], v238, s[46:47]
	global_load_dwordx4 v[172:175], v238, s[46:47] offset:128
	v_add_u32_e32 v238, 0x1c000, v220
	global_load_dwordx4 v[144:147], v238, s[46:47]
	global_load_dwordx4 v[176:179], v238, s[46:47] offset:128
	v_add_u32_e32 v238, 0x23000, v220
	global_load_dwordx4 v[148:151], v238, s[46:47]
	global_load_dwordx4 v[180:183], v238, s[46:47] offset:128
	v_add_u32_e32 v238, 0x2a000, v220
	global_load_dwordx4 v[152:155], v238, s[46:47]
	global_load_dwordx4 v[184:187], v238, s[46:47] offset:128
	v_add_u32_e32 v238, 0x31000, v220
	global_load_dwordx4 v[156:159], v238, s[46:47]
	global_load_dwordx4 v[188:191], v238, s[46:47] offset:128
	global_load_dwordx4 v[212:215], v222, s[48:49]
	global_load_dwordx4 v[216:219], v222, s[48:49] offset:16
	s_waitcnt vmcnt(36)
; __device__ __forceinline__ unsigned pk4_fp8(float a, float b, float c, float d) {
;     a = __builtin_amdgcn_fmed3f(a, -448.f, 448.f); b = __builtin_amdgcn_fmed3f(b, -448.f, 448.f); c = __builtin_amdgcn_fmed3f(c, -448.f, 448.f); d = __builtin_amdgcn_fmed3f(d, -448.f, 448.f);
;     unsigned w = 0u; w = __builtin_amdgcn_cvt_pk_fp8_f32(a, b, w, false); w = __builtin_amdgcn_cvt_pk_fp8_f32(c, d, w, true); return w;
; }
; __device__ __forceinline__ void titem_process(const TItem& t, const f32x4 (&v)[2][8], const f32x4 (&g)[2], int lane) {
;     const int n4 = lane & 7, kr = lane >> 3;
;     float s[8];
; #pragma unroll
;     for (int j = 0; j < 8; ++j) s[j] = t.gain ? g[j >> 2][j & 3] * t.scale : t.scale;
;     if (t.fp8 == 1) {
; #pragma unroll
;         for (int h = 0; h < 2; ++h)
; #pragma unroll
;             for (int i = 0; i < 4; ++i) { u32x2 o; o.x = epi::pk4_fp8(v[h][0][i] * s[0], v[h][1][i] * s[1], v[h][2][i] * s[2], v[h][3][i] * s[3]); o.y = epi::pk4_fp8(v[h][4][i] * s[4], v[h][5][i] * s[5], v[h][6][i] * s[6], v[h][7][i] * s[7]);
;                 __builtin_nontemporal_store(o, (u32x2*)(t.dst + (size_t)(32 * h + 4 * n4 + i) * t.ldwt + 8 * kr)); }
	v_mul_f32_e32 v226, 0x43800000, v192
	v_mul_f32_e32 v227, 0x43800000, v193
	v_mul_f32_e32 v228, 0x43800000, v194
	v_mul_f32_e32 v229, 0x43800000, v195
	v_mul_f32_e32 v230, 0x43800000, v196
	v_mul_f32_e32 v231, 0x43800000, v197
	v_mul_f32_e32 v232, 0x43800000, v198
	v_mul_f32_e32 v233, 0x43800000, v199
	v_pk_mul_f32 v[0:1], v[0:1], v[226:227] op_sel:[0,0] op_sel_hi:[1,0]
	v_pk_mul_f32 v[4:5], v[4:5], v[226:227] op_sel:[0,1] op_sel_hi:[1,1]
	v_pk_mul_f32 v[8:9], v[8:9], v[228:229] op_sel:[0,0] op_sel_hi:[1,0]
	v_pk_mul_f32 v[12:13], v[12:13], v[228:229] op_sel:[0,1] op_sel_hi:[1,1]
	v_pk_mul_f32 v[16:17], v[16:17], v[230:231] op_sel:[0,0] op_sel_hi:[1,0]
	v_pk_mul_f32 v[20:21], v[20:21], v[230:231] op_sel:[0,1] op_sel_hi:[1,1]
	v_pk_mul_f32 v[24:25], v[24:25], v[232:233] op_sel:[0,0] op_sel_hi:[1,0]
	v_pk_mul_f32 v[28:29], v[28:29], v[232:233] op_sel:[0,1] op_sel_hi:[1,1]
	v_pk_mul_f32 v[2:3], v[2:3], v[226:227] op_sel:[0,0] op_sel_hi:[1,0]
	v_pk_mul_f32 v[6:7], v[6:7], v[226:227] op_sel:[0,1] op_sel_hi:[1,1]
	v_pk_mul_f32 v[10:11], v[10:11], v[228:229] op_sel:[0,0] op_sel_hi:[1,0]
	v_pk_mul_f32 v[14:15], v[14:15], v[228:229] op_sel:[0,1] op_sel_hi:[1,1]
	v_pk_mul_f32 v[18:19], v[18:19], v[230:231] op_sel:[0,0] op_sel_hi:[1,0]
	v_pk_mul_f32 v[22:23], v[22:23], v[230:231] op_sel:[0,1] op_sel_hi:[1,1]
	v_pk_mul_f32 v[26:27], v[26:27], v[232:233] op_sel:[0,0] op_sel_hi:[1,0]
	v_pk_mul_f32 v[30:31], v[30:31], v[232:233] op_sel:[0,1] op_sel_hi:[1,1]
	v_pk_mul_f32 v[32:33], v[32:33], v[226:227] op_sel:[0,0] op_sel_hi:[1,0]
	v_pk_mul_f32 v[36:37], v[36:37], v[226:227] op_sel:[0,1] op_sel_hi:[1,1]
	v_pk_mul_f32 v[40:41], v[40:41], v[228:229] op_sel:[0,0] op_sel_hi:[1,0]
	v_pk_mul_f32 v[44:45], v[44:45], v[228:229] op_sel:[0,1] op_sel_hi:[1,1]
	v_pk_mul_f32 v[48:49], v[48:49], v[230:231] op_sel:[0,0] op_sel_hi:[1,0]
	v_pk_mul_f32 v[52:53], v[52:53], v[230:231] op_sel:[0,1] op_sel_hi:[1,1]
	v_pk_mul_f32 v[56:57], v[56:57], v[232:233] op_sel:[0,0] op_sel_hi:[1,0]
	v_pk_mul_f32 v[60:61], v[60:61], v[232:233] op_sel:[0,1] op_sel_hi:[1,1]
	v_pk_mul_f32 v[34:35], v[34:35], v[226:227] op_sel:[0,0] op_sel_hi:[1,0]
	v_pk_mul_f32 v[38:39], v[38:39], v[226:227] op_sel:[0,1] op_sel_hi:[1,1]
	v_pk_mul_f32 v[42:43], v[42:43], v[228:229] op_sel:[0,0] op_sel_hi:[1,0]
	v_pk_mul_f32 v[46:47], v[46:47], v[228:229] op_sel:[0,1] op_sel_hi:[1,1]
	v_pk_mul_f32 v[50:51], v[50:51], v[230:231] op_sel:[0,0] op_sel_hi:[1,0]
	v_pk_mul_f32 v[54:55], v[54:55], v[230:231] op_sel:[0,1] op_sel_hi:[1,1]
	v_pk_mul_f32 v[58:59], v[58:59], v[232:233] op_sel:[0,0] op_sel_hi:[1,0]
	v_pk_mul_f32 v[62:63], v[62:63], v[232:233] op_sel:[0,1] op_sel_hi:[1,1]
	v_med3_f32 v0, v0, s33, v225
	v_med3_f32 v1, v1, s33, v225
	v_med3_f32 v2, v2, s33, v225
	v_med3_f32 v3, v3, s33, v225
	v_med3_f32 v4, v4, s33, v225
	v_med3_f32 v5, v5, s33, v225
	v_med3_f32 v6, v6, s33, v225
	v_med3_f32 v7, v7, s33, v225
	v_med3_f32 v8, v8, s33, v225
	v_med3_f32 v9, v9, s33, v225
	v_med3_f32 v10, v10, s33, v225
	v_med3_f32 v11, v11, s33, v225
	v_med3_f32 v12, v12, s33, v225
	v_med3_f32 v13, v13, s33, v225
	v_med3_f32 v14, v14, s33, v225
	v_med3_f32 v15, v15, s33, v225
	v_med3_f32 v16, v16, s33, v225
	v_med3_f32 v17, v17, s33, v225
	v_med3_f32 v18, v18, s33, v225
	v_med3_f32 v19, v19, s33, v225
	v_med3_f32 v20, v20, s33, v225
	v_med3_f32 v21, v21, s33, v225
	v_med3_f32 v22, v22, s33, v225
	v_med3_f32 v23, v23, s33, v225
	v_med3_f32 v24, v24, s33, v225
	v_med3_f32 v25, v25, s33, v225
	v_med3_f32 v26, v26, s33, v225
	v_med3_f32 v27, v27, s33, v225
	v_med3_f32 v28, v28, s33, v225
	v_med3_f32 v29, v29, s33, v225
	v_med3_f32 v30, v30, s33, v225
	v_med3_f32 v31, v31, s33, v225
	v_med3_f32 v32, v32, s33, v225
	v_med3_f32 v33, v33, s33, v225
	v_med3_f32 v34, v34, s33, v225
	v_med3_f32 v35, v35, s33, v225
	v_med3_f32 v36, v36, s33, v225
	v_med3_f32 v37, v37, s33, v225
	v_med3_f32 v38, v38, s33, v225
	v_med3_f32 v39, v39, s33, v225
	v_med3_f32 v40, v40, s33, v225
	v_med3_f32 v41, v41, s33, v225
	v_med3_f32 v42, v42, s33, v225
	v_med3_f32 v43, v43, s33, v225
	v_med3_f32 v44, v44, s33, v225
	v_med3_f32 v45, v45, s33, v225
	v_med3_f32 v46, v46, s33, v225
	v_med3_f32 v47, v47, s33, v225
	v_med3_f32 v48, v48, s33, v225
	v_med3_f32 v49, v49, s33, v225
	v_med3_f32 v50, v50, s33, v225
	v_med3_f32 v51, v51, s33, v225
	v_med3_f32 v52, v52, s33, v225
	v_med3_f32 v53, v53, s33, v225
	v_med3_f32 v54, v54, s33, v225
	v_med3_f32 v55, v55, s33, v225
	v_med3_f32 v56, v56, s33, v225
	v_med3_f32 v57, v57, s33, v225
	v_med3_f32 v58, v58, s33, v225
	v_med3_f32 v59, v59, s33, v225
	v_med3_f32 v60, v60, s33, v225
	v_med3_f32 v61, v61, s33, v225
	v_med3_f32 v62, v62, s33, v225
	v_med3_f32 v63, v63, s33, v225
	v_cvt_pk_fp8_f32 v234, v0, v4
	v_cvt_pk_fp8_f32 v235, v16, v20
	v_cvt_pk_fp8_f32 v234, v8, v12 op_sel:[0,0,1]
	v_cvt_pk_fp8_f32 v235, v24, v28 op_sel:[0,0,1]
	s_nop 0
	global_store_dwordx2 v223, v[234:235], s[38:39] nt
	v_cvt_pk_fp8_f32 v236, v1, v5
	v_cvt_pk_fp8_f32 v237, v17, v21
	v_cvt_pk_fp8_f32 v236, v9, v13 op_sel:[0,0,1]
	v_cvt_pk_fp8_f32 v237, v25, v29 op_sel:[0,0,1]
	v_add_u32_e32 v238, 0x800, v223
	global_store_dwordx2 v238, v[236:237], s[38:39] nt
	v_cvt_pk_fp8_f32 v234, v2, v6
	v_cvt_pk_fp8_f32 v235, v18, v22
	v_cvt_pk_fp8_f32 v234, v10, v14 op_sel:[0,0,1]
	v_cvt_pk_fp8_f32 v235, v26, v30 op_sel:[0,0,1]
	v_add_u32_e32 v238, 0x1000, v223
	global_store_dwordx2 v238, v[234:235], s[38:39] nt
	v_cvt_pk_fp8_f32 v236, v3, v7
	v_cvt_pk_fp8_f32 v237, v19, v23
	v_cvt_pk_fp8_f32 v236, v11, v15 op_sel:[0,0,1]
	v_cvt_pk_fp8_f32 v237, v27, v31 op_sel:[0,0,1]
	v_add_u32_e32 v238, 0x1800, v223
	global_store_dwordx2 v238, v[236:237], s[38:39] nt
	v_cvt_pk_fp8_f32 v234, v32, v36
	v_cvt_pk_fp8_f32 v235, v48, v52
	v_cvt_pk_fp8_f32 v234, v40, v44 op_sel:[0,0,1]
	v_cvt_pk_fp8_f32 v235, v56, v60 op_sel:[0,0,1]
	v_add_u32_e32 v238, 0x10000, v223
	global_store_dwordx2 v238, v[234:235], s[38:39] nt
	v_cvt_pk_fp8_f32 v236, v33, v37
	v_cvt_pk_fp8_f32 v237, v49, v53
	v_cvt_pk_fp8_f32 v236, v41, v45 op_sel:[0,0,1]
	v_cvt_pk_fp8_f32 v237, v57, v61 op_sel:[0,0,1]
	v_add_u32_e32 v238, 0x10800, v223
	global_store_dwordx2 v238, v[236:237], s[38:39] nt
	v_cvt_pk_fp8_f32 v234, v34, v38
	v_cvt_pk_fp8_f32 v235, v50, v54
	v_cvt_pk_fp8_f32 v234, v42, v46 op_sel:[0,0,1]
	v_cvt_pk_fp8_f32 v235, v58, v62 op_sel:[0,0,1]
	v_add_u32_e32 v238, 0x11000, v223
	global_store_dwordx2 v238, v[234:235], s[38:39] nt
	v_cvt_pk_fp8_f32 v236, v35, v39
	v_cvt_pk_fp8_f32 v237, v51, v55
	v_cvt_pk_fp8_f32 v236, v43, v47 op_sel:[0,0,1]
	v_cvt_pk_fp8_f32 v237, v59, v63 op_sel:[0,0,1]
	v_add_u32_e32 v238, 0x11800, v223
	global_store_dwordx2 v238, v[236:237], s[38:39] nt
	s_mov_b32 s27, 1
	s_mov_b32 s30, 9
